# S5-out item: 64 serialized carry-state loads (load/vmcnt0/use chain) batched into 2 groups of 32 into free VGPRs
# speedup vs baseline: 1.0132x; 1.0132x over previous
.LBB0_447:
	s_and_b32 s2, s12, 60
	s_or_b32 s15, s2, s0
	s_lshr_b32 s2, s14, 3
	s_and_b32 s2, s2, 0x7fffffe
	s_add_i32 s2, s2, s1
	v_mov_b32_e32 v132, v136
	s_lshl_b32 s2, s2, 5
	s_lshl_b32 s88, s15, 5
	v_and_or_b32 v3, v132, 31, s2
	v_lshlrev_b32_e32 v130, 4, v3
	v_ashrrev_i32_e32 v131, 31, v130
	v_ashrrev_i32_e32 v2, 5, v132
	v_lshlrev_b64 v[0:1], 13, v[130:131]
	v_lshl_add_u64 v[0:1], s[90:91], 0, v[0:1]
	v_lshlrev_b32_e32 v4, 3, v2
	v_lshl_add_u64 v[0:1], v[0:1], 0, s[88:89]
	v_ashrrev_i32_e32 v5, 31, v4
	v_lshl_add_u64 v[0:1], v[4:5], 1, v[0:1]
	v_add_co_u32_e32 v6, vcc, s68, v0
	v_max_i32_e32 v96, 1, v3
	s_nop 0
	v_addc_co_u32_e32 v7, vcc, 0, v1, vcc
	global_load_dwordx4 v[32:35], v[6:7], off offset:2048
	v_add_co_u32_e32 v6, vcc, s69, v0
	v_ashrrev_i32_e32 v133, 31, v132
	s_nop 0
	v_addc_co_u32_e32 v7, vcc, 0, v1, vcc
	global_load_dwordx4 v[36:39], v[6:7], off offset:2048
	v_add_co_u32_e32 v6, vcc, s6, v0
	s_mul_i32 s88, s15, 0x3000
	s_nop 0
	v_addc_co_u32_e32 v7, vcc, 0, v1, vcc
	global_load_dwordx4 v[40:43], v[6:7], off offset:2048
	v_add_co_u32_e32 v6, vcc, s7, v0
	s_lshl_b32 s16, s15, 4
	s_nop 0
	v_addc_co_u32_e32 v7, vcc, 0, v1, vcc
	global_load_dwordx4 v[44:47], v[6:7], off offset:2048
	v_add_co_u32_e32 v6, vcc, s17, v0
	v_lshl_add_u32 v134, v2, 2, s16
	s_nop 0
	v_addc_co_u32_e32 v7, vcc, 0, v1, vcc
	global_load_dwordx4 v[48:51], v[6:7], off offset:2048
	v_add_co_u32_e32 v6, vcc, s18, v0
	s_nop 1
	v_addc_co_u32_e32 v7, vcc, 0, v1, vcc
	global_load_dwordx4 v[52:55], v[6:7], off offset:2048
	v_add_co_u32_e32 v6, vcc, s21, v0
	s_nop 1
	v_addc_co_u32_e32 v7, vcc, 0, v1, vcc
	global_load_dwordx4 v[56:59], v[6:7], off offset:2048
	v_add_co_u32_e32 v6, vcc, s24, v0
	s_nop 1
	v_addc_co_u32_e32 v7, vcc, 0, v1, vcc
	global_load_dwordx4 v[60:63], v[6:7], off offset:2048
	v_add_co_u32_e32 v6, vcc, s25, v0
	s_nop 1
	v_addc_co_u32_e32 v7, vcc, 0, v1, vcc
	global_load_dwordx4 v[64:67], v[6:7], off offset:2048
	v_add_co_u32_e32 v6, vcc, s93, v0
	s_nop 1
	v_addc_co_u32_e32 v7, vcc, 0, v1, vcc
	global_load_dwordx4 v[68:71], v[6:7], off offset:2048
	v_add_co_u32_e32 v6, vcc, s19, v0
	s_nop 1
	v_addc_co_u32_e32 v7, vcc, 0, v1, vcc
	global_load_dwordx4 v[72:75], v[6:7], off offset:2048
	v_add_co_u32_e32 v6, vcc, s20, v0
	s_nop 1
	v_addc_co_u32_e32 v7, vcc, 0, v1, vcc
	global_load_dwordx4 v[76:79], v[6:7], off offset:2048
	v_add_co_u32_e32 v6, vcc, s22, v0
	s_nop 1
	v_addc_co_u32_e32 v7, vcc, 0, v1, vcc
	global_load_dwordx4 v[80:83], v[6:7], off offset:2048
	v_add_co_u32_e32 v6, vcc, s23, v0
	s_nop 1
	v_addc_co_u32_e32 v7, vcc, 0, v1, vcc
	global_load_dwordx4 v[84:87], v[6:7], off offset:2048
	v_add_co_u32_e32 v6, vcc, s28, v0
	s_nop 1
	v_addc_co_u32_e32 v7, vcc, 0, v1, vcc
	v_add_co_u32_e32 v0, vcc, s29, v0
	global_load_dwordx4 v[88:91], v[6:7], off offset:2048
	s_nop 0
	v_addc_co_u32_e32 v1, vcc, 0, v1, vcc
	global_load_dwordx4 v[92:95], v[0:1], off offset:2048
	v_lshl_add_u32 v0, s15, 7, v4
	v_ashrrev_i32_e32 v1, 31, v0
	v_lshlrev_b64 v[0:1], 12, v[0:1]
	v_lshl_add_u64 v[0:1], s[8:9], 0, v[0:1]
	v_lshl_add_u64 v[0:1], v[96:97], 2, v[0:1]
	v_cmp_lt_i32_e32 vcc, 0, v3
	global_load_dword v138, v[0:1], off offset:-4
	global_load_dword v139, v[0:1], off offset:4092
	v_add_co_u32_e64 v4, s[2:3], s81, v0
	s_nop 1
	v_addc_co_u32_e64 v5, s[2:3], 0, v1, s[2:3]
	global_load_dword v140, v[4:5], off offset:4092
	v_add_co_u32_e64 v4, s[2:3], s43, v0
	s_nop 1
	v_addc_co_u32_e64 v5, s[2:3], 0, v1, s[2:3]
	global_load_dword v141, v[4:5], off offset:4092
	v_add_co_u32_e64 v4, s[2:3], s72, v0
	s_nop 1
	v_addc_co_u32_e64 v5, s[2:3], 0, v1, s[2:3]
	global_load_dword v142, v[4:5], off offset:4092
	v_add_co_u32_e64 v4, s[2:3], s54, v0
	s_nop 1
	v_addc_co_u32_e64 v5, s[2:3], 0, v1, s[2:3]
	global_load_dword v143, v[4:5], off offset:4092
	v_add_co_u32_e64 v4, s[2:3], s77, v0
	s_nop 1
	v_addc_co_u32_e64 v5, s[2:3], 0, v1, s[2:3]
	global_load_dword v144, v[4:5], off offset:4092
	s_movk_i32 s2, 0x6000
	v_add_co_u32_e64 v4, s[2:3], s2, v0
	s_nop 1
	v_addc_co_u32_e64 v5, s[2:3], 0, v1, s[2:3]
	global_load_dword v145, v[4:5], off offset:4092
	s_mov_b32 s2, 0xf000
	v_add_co_u32_e64 v4, s[2:3], s2, v0
	s_nop 1
	v_addc_co_u32_e64 v5, s[2:3], 0, v1, s[2:3]
	global_load_dword v146, v[4:5], off offset:4092
	v_add_co_u32_e64 v4, s[2:3], s30, v0
	s_nop 1
	v_addc_co_u32_e64 v5, s[2:3], 0, v1, s[2:3]
	global_load_dword v147, v[4:5], off offset:4092
	v_add_co_u32_e64 v4, s[2:3], s36, v0
	s_nop 1
	v_addc_co_u32_e64 v5, s[2:3], 0, v1, s[2:3]
	global_load_dword v148, v[4:5], off offset:4092
	s_mov_b32 s2, 0x12000
	v_add_co_u32_e64 v4, s[2:3], s2, v0
	s_nop 1
	v_addc_co_u32_e64 v5, s[2:3], 0, v1, s[2:3]
	global_load_dword v149, v[4:5], off offset:4092
	v_add_co_u32_e64 v4, s[2:3], s37, v0
	s_nop 1
	v_addc_co_u32_e64 v5, s[2:3], 0, v1, s[2:3]
	global_load_dword v150, v[4:5], off offset:4092
	s_mov_b32 s2, 0x14000
	v_add_co_u32_e64 v4, s[2:3], s2, v0
	s_nop 1
	v_addc_co_u32_e64 v5, s[2:3], 0, v1, s[2:3]
	global_load_dword v151, v[4:5], off offset:4092
	s_mov_b32 s2, 0x15000
	v_add_co_u32_e64 v4, s[2:3], s2, v0
	s_nop 1
	v_addc_co_u32_e64 v5, s[2:3], 0, v1, s[2:3]
	global_load_dword v152, v[4:5], off offset:4092
	s_mov_b32 s2, 0x16000
	v_add_co_u32_e64 v4, s[2:3], s2, v0
	s_nop 1
	v_addc_co_u32_e64 v5, s[2:3], 0, v1, s[2:3]
	global_load_dword v153, v[4:5], off offset:4092
	s_mov_b32 s2, 0x1f000
	v_add_co_u32_e64 v4, s[2:3], s2, v0
	s_nop 1
	v_addc_co_u32_e64 v5, s[2:3], 0, v1, s[2:3]
	global_load_dword v154, v[4:5], off offset:4092
	v_add_co_u32_e64 v4, s[2:3], s31, v0
	s_nop 1
	v_addc_co_u32_e64 v5, s[2:3], 0, v1, s[2:3]
	global_load_dword v155, v[4:5], off offset:4092
	s_mov_b32 s2, 0x21000
	v_add_co_u32_e64 v4, s[2:3], s2, v0
	s_nop 1
	v_addc_co_u32_e64 v5, s[2:3], 0, v1, s[2:3]
	global_load_dword v156, v[4:5], off offset:4092
	s_mov_b32 s2, 0x22000
	v_add_co_u32_e64 v4, s[2:3], s2, v0
	s_nop 1
	v_addc_co_u32_e64 v5, s[2:3], 0, v1, s[2:3]
	global_load_dword v157, v[4:5], off offset:4092
	s_mov_b32 s2, 0x23000
	v_add_co_u32_e64 v4, s[2:3], s2, v0
	s_nop 1
	v_addc_co_u32_e64 v5, s[2:3], 0, v1, s[2:3]
	global_load_dword v158, v[4:5], off offset:4092
	s_mov_b32 s2, 0x24000
	v_add_co_u32_e64 v4, s[2:3], s2, v0
	s_nop 1
	v_addc_co_u32_e64 v5, s[2:3], 0, v1, s[2:3]
	global_load_dword v159, v[4:5], off offset:4092
	s_mov_b32 s2, 0x25000
	v_add_co_u32_e64 v4, s[2:3], s2, v0
	s_nop 1
	v_addc_co_u32_e64 v5, s[2:3], 0, v1, s[2:3]
	global_load_dword v160, v[4:5], off offset:4092
	s_mov_b32 s2, 0x26000
	v_add_co_u32_e64 v4, s[2:3], s2, v0
	s_nop 1
	v_addc_co_u32_e64 v5, s[2:3], 0, v1, s[2:3]
	global_load_dword v161, v[4:5], off offset:4092
	s_mov_b32 s2, 0x2f000
	v_add_co_u32_e64 v4, s[2:3], s2, v0
	s_nop 1
	v_addc_co_u32_e64 v5, s[2:3], 0, v1, s[2:3]
	s_mov_b32 s2, 0x30000
	global_load_dword v162, v[4:5], off offset:4092
	v_add_co_u32_e64 v4, s[2:3], s2, v0
	s_nop 1
	v_addc_co_u32_e64 v5, s[2:3], 0, v1, s[2:3]
	global_load_dword v163, v[4:5], off offset:4092
	v_add_co_u32_e64 v4, s[2:3], s48, v0
	s_nop 1
	v_addc_co_u32_e64 v5, s[2:3], 0, v1, s[2:3]
	global_load_dword v164, v[4:5], off offset:4092
	s_mov_b32 s2, 0x32000
	v_add_co_u32_e64 v4, s[2:3], s2, v0
	s_nop 1
	v_addc_co_u32_e64 v5, s[2:3], 0, v1, s[2:3]
	global_load_dword v165, v[4:5], off offset:4092
	v_add_co_u32_e64 v4, s[2:3], s49, v0
	s_nop 1
	v_addc_co_u32_e64 v5, s[2:3], 0, v1, s[2:3]
	global_load_dword v166, v[4:5], off offset:4092
	s_mov_b32 s2, 0x34000
	v_add_co_u32_e64 v4, s[2:3], s2, v0
	s_nop 1
	v_addc_co_u32_e64 v5, s[2:3], 0, v1, s[2:3]
	global_load_dword v167, v[4:5], off offset:4092
	s_mov_b32 s2, 0x35000
	v_add_co_u32_e64 v4, s[2:3], s2, v0
	s_nop 1
	v_addc_co_u32_e64 v5, s[2:3], 0, v1, s[2:3]
	global_load_dword v168, v[4:5], off offset:4092
	s_mov_b32 s2, 0x36000
	v_add_co_u32_e64 v4, s[2:3], s2, v0
	s_nop 1
	v_addc_co_u32_e64 v5, s[2:3], 0, v1, s[2:3]
	global_load_dword v169, v[4:5], off offset:4092
	s_waitcnt vmcnt(0)
	v_cndmask_b32_e32 v3, 0, v138, vcc
	v_cndmask_b32_e32 v6, 0, v139, vcc
	v_cndmask_b32_e32 v7, 0, v140, vcc
	v_cndmask_b32_e32 v8, 0, v141, vcc
	v_cndmask_b32_e32 v9, 0, v142, vcc
	v_cndmask_b32_e32 v10, 0, v143, vcc
	v_cndmask_b32_e32 v11, 0, v144, vcc
	v_cvt_pk_bf16_f32 v98, v3, v6
	v_cvt_pk_bf16_f32 v99, v7, v8
	v_cvt_pk_bf16_f32 v100, v9, v10
	v_cndmask_b32_e32 v4, 0, v145, vcc
	v_cvt_pk_bf16_f32 v101, v11, v4
	v_cndmask_b32_e32 v3, 0, v146, vcc
	v_cndmask_b32_e32 v6, 0, v147, vcc
	v_cndmask_b32_e32 v7, 0, v148, vcc
	v_cndmask_b32_e32 v8, 0, v149, vcc
	v_cndmask_b32_e32 v9, 0, v150, vcc
	v_cndmask_b32_e32 v10, 0, v151, vcc
	v_cndmask_b32_e32 v11, 0, v152, vcc
	v_cvt_pk_bf16_f32 v102, v3, v6
	v_cvt_pk_bf16_f32 v103, v7, v8
	v_cvt_pk_bf16_f32 v104, v9, v10
	v_cndmask_b32_e32 v4, 0, v153, vcc
	v_cvt_pk_bf16_f32 v105, v11, v4
	v_cndmask_b32_e32 v3, 0, v154, vcc
	v_cndmask_b32_e32 v6, 0, v155, vcc
	v_cndmask_b32_e32 v7, 0, v156, vcc
	v_cndmask_b32_e32 v8, 0, v157, vcc
	v_cndmask_b32_e32 v9, 0, v158, vcc
	v_cndmask_b32_e32 v10, 0, v159, vcc
	v_cndmask_b32_e32 v11, 0, v160, vcc
	v_cvt_pk_bf16_f32 v106, v3, v6
	v_cvt_pk_bf16_f32 v107, v7, v8
	v_cvt_pk_bf16_f32 v108, v9, v10
	v_cndmask_b32_e32 v4, 0, v161, vcc
	v_cvt_pk_bf16_f32 v109, v11, v4
	v_cndmask_b32_e32 v3, 0, v162, vcc
	v_cndmask_b32_e32 v6, 0, v163, vcc
	v_cndmask_b32_e32 v7, 0, v164, vcc
	v_cndmask_b32_e32 v8, 0, v165, vcc
	v_cndmask_b32_e32 v9, 0, v166, vcc
	v_cndmask_b32_e32 v10, 0, v167, vcc
	v_cndmask_b32_e32 v11, 0, v168, vcc
	v_cvt_pk_bf16_f32 v110, v3, v6
	v_cvt_pk_bf16_f32 v111, v7, v8
	v_cvt_pk_bf16_f32 v112, v9, v10
	v_cndmask_b32_e32 v4, 0, v169, vcc
	v_cvt_pk_bf16_f32 v113, v11, v4
	s_mov_b32 s2, 0x3f000
	v_add_co_u32_e64 v4, s[2:3], s2, v0
	s_nop 1
	v_addc_co_u32_e64 v5, s[2:3], 0, v1, s[2:3]
	global_load_dword v138, v[4:5], off offset:4092
	v_add_co_u32_e64 v4, s[2:3], s52, v0
	s_nop 1
	v_addc_co_u32_e64 v5, s[2:3], 0, v1, s[2:3]
	global_load_dword v139, v[4:5], off offset:4092
	s_mov_b32 s2, 0x41000
	v_add_co_u32_e64 v4, s[2:3], s2, v0
	s_nop 1
	v_addc_co_u32_e64 v5, s[2:3], 0, v1, s[2:3]
	global_load_dword v140, v[4:5], off offset:4092
	s_mov_b32 s2, 0x42000
	v_add_co_u32_e64 v4, s[2:3], s2, v0
	s_nop 1
	v_addc_co_u32_e64 v5, s[2:3], 0, v1, s[2:3]
	global_load_dword v141, v[4:5], off offset:4092
	s_mov_b32 s2, 0x43000
	v_add_co_u32_e64 v4, s[2:3], s2, v0
	s_nop 1
	v_addc_co_u32_e64 v5, s[2:3], 0, v1, s[2:3]
	global_load_dword v142, v[4:5], off offset:4092
	s_mov_b32 s2, 0x44000
	v_add_co_u32_e64 v4, s[2:3], s2, v0
	s_nop 1
	v_addc_co_u32_e64 v5, s[2:3], 0, v1, s[2:3]
	global_load_dword v143, v[4:5], off offset:4092
	s_mov_b32 s2, 0x45000
	v_add_co_u32_e64 v4, s[2:3], s2, v0
	s_nop 1
	v_addc_co_u32_e64 v5, s[2:3], 0, v1, s[2:3]
	global_load_dword v144, v[4:5], off offset:4092
	s_mov_b32 s2, 0x46000
	v_add_co_u32_e64 v4, s[2:3], s2, v0
	s_nop 1
	v_addc_co_u32_e64 v5, s[2:3], 0, v1, s[2:3]
	global_load_dword v145, v[4:5], off offset:4092
	s_mov_b32 s2, 0x4f000
	v_add_co_u32_e64 v4, s[2:3], s2, v0
	s_nop 1
	v_addc_co_u32_e64 v5, s[2:3], 0, v1, s[2:3]
	s_mov_b32 s2, 0x50000
	global_load_dword v146, v[4:5], off offset:4092
	v_add_co_u32_e64 v4, s[2:3], s2, v0
	s_nop 1
	v_addc_co_u32_e64 v5, s[2:3], 0, v1, s[2:3]
	global_load_dword v147, v[4:5], off offset:4092
	v_add_co_u32_e64 v4, s[2:3], s53, v0
	s_nop 1
	v_addc_co_u32_e64 v5, s[2:3], 0, v1, s[2:3]
	global_load_dword v148, v[4:5], off offset:4092
	s_mov_b32 s2, 0x52000
	v_add_co_u32_e64 v4, s[2:3], s2, v0
	s_nop 1
	v_addc_co_u32_e64 v5, s[2:3], 0, v1, s[2:3]
	global_load_dword v149, v[4:5], off offset:4092
	v_add_co_u32_e64 v4, s[2:3], s56, v0
	s_nop 1
	v_addc_co_u32_e64 v5, s[2:3], 0, v1, s[2:3]
	global_load_dword v150, v[4:5], off offset:4092
	s_mov_b32 s2, 0x54000
	v_add_co_u32_e64 v4, s[2:3], s2, v0
	s_nop 1
	v_addc_co_u32_e64 v5, s[2:3], 0, v1, s[2:3]
	global_load_dword v151, v[4:5], off offset:4092
	s_mov_b32 s2, 0x55000
	v_add_co_u32_e64 v4, s[2:3], s2, v0
	s_nop 1
	v_addc_co_u32_e64 v5, s[2:3], 0, v1, s[2:3]
	global_load_dword v152, v[4:5], off offset:4092
	s_mov_b32 s2, 0x56000
	v_add_co_u32_e64 v4, s[2:3], s2, v0
	s_nop 1
	v_addc_co_u32_e64 v5, s[2:3], 0, v1, s[2:3]
	global_load_dword v153, v[4:5], off offset:4092
	s_mov_b32 s2, 0x5f000
	v_add_co_u32_e64 v4, s[2:3], s2, v0
	s_nop 1
	v_addc_co_u32_e64 v5, s[2:3], 0, v1, s[2:3]
	global_load_dword v154, v[4:5], off offset:4092
	v_add_co_u32_e64 v4, s[2:3], s57, v0
	s_nop 1
	v_addc_co_u32_e64 v5, s[2:3], 0, v1, s[2:3]
	global_load_dword v155, v[4:5], off offset:4092
	s_mov_b32 s2, 0x61000
	v_add_co_u32_e64 v4, s[2:3], s2, v0
	s_nop 1
	v_addc_co_u32_e64 v5, s[2:3], 0, v1, s[2:3]
	global_load_dword v156, v[4:5], off offset:4092
	s_mov_b32 s2, 0x62000
	v_add_co_u32_e64 v4, s[2:3], s2, v0
	s_nop 1
	v_addc_co_u32_e64 v5, s[2:3], 0, v1, s[2:3]
	global_load_dword v157, v[4:5], off offset:4092
	s_mov_b32 s2, 0x63000
	v_add_co_u32_e64 v4, s[2:3], s2, v0
	s_nop 1
	v_addc_co_u32_e64 v5, s[2:3], 0, v1, s[2:3]
	global_load_dword v158, v[4:5], off offset:4092
	s_mov_b32 s2, 0x64000
	v_add_co_u32_e64 v4, s[2:3], s2, v0
	s_nop 1
	v_addc_co_u32_e64 v5, s[2:3], 0, v1, s[2:3]
	global_load_dword v159, v[4:5], off offset:4092
	s_mov_b32 s2, 0x65000
	v_add_co_u32_e64 v4, s[2:3], s2, v0
	s_nop 1
	v_addc_co_u32_e64 v5, s[2:3], 0, v1, s[2:3]
	global_load_dword v160, v[4:5], off offset:4092
	s_mov_b32 s2, 0x66000
	v_add_co_u32_e64 v4, s[2:3], s2, v0
	s_nop 1
	v_addc_co_u32_e64 v5, s[2:3], 0, v1, s[2:3]
	global_load_dword v161, v[4:5], off offset:4092
	s_mov_b32 s2, 0x6f000
	v_add_co_u32_e64 v4, s[2:3], s2, v0
	s_nop 1
	v_addc_co_u32_e64 v5, s[2:3], 0, v1, s[2:3]
	s_mov_b32 s2, 0x70000
	global_load_dword v162, v[4:5], off offset:4092
	v_add_co_u32_e64 v4, s[2:3], s2, v0
	s_nop 1
	v_addc_co_u32_e64 v5, s[2:3], 0, v1, s[2:3]
	global_load_dword v163, v[4:5], off offset:4092
	v_add_co_u32_e64 v4, s[2:3], s59, v0
	s_nop 1
	v_addc_co_u32_e64 v5, s[2:3], 0, v1, s[2:3]
	global_load_dword v164, v[4:5], off offset:4092
	s_mov_b32 s2, 0x72000
	v_add_co_u32_e64 v4, s[2:3], s2, v0
	s_nop 1
	v_addc_co_u32_e64 v5, s[2:3], 0, v1, s[2:3]
	global_load_dword v165, v[4:5], off offset:4092
	v_add_co_u32_e64 v4, s[2:3], s60, v0
	s_nop 1
	v_addc_co_u32_e64 v5, s[2:3], 0, v1, s[2:3]
	global_load_dword v166, v[4:5], off offset:4092
	s_mov_b32 s2, 0x74000
	v_add_co_u32_e64 v4, s[2:3], s2, v0
	s_nop 1
	v_addc_co_u32_e64 v5, s[2:3], 0, v1, s[2:3]
	global_load_dword v167, v[4:5], off offset:4092
	s_mov_b32 s2, 0x75000
	v_add_co_u32_e64 v4, s[2:3], s2, v0
	s_nop 1
	v_addc_co_u32_e64 v5, s[2:3], 0, v1, s[2:3]
	s_mov_b32 s2, 0x76000
	s_nop 0
	v_add_co_u32_e64 v0, s[2:3], s2, v0
	global_load_dword v168, v[4:5], off offset:4092
	s_nop 0
	v_addc_co_u32_e64 v1, s[2:3], 0, v1, s[2:3]
	global_load_dword v169, v[0:1], off offset:4092
	s_waitcnt vmcnt(0)
	v_cndmask_b32_e32 v3, 0, v138, vcc
	v_cndmask_b32_e32 v6, 0, v139, vcc
	v_cndmask_b32_e32 v7, 0, v140, vcc
	v_cndmask_b32_e32 v8, 0, v141, vcc
	v_cndmask_b32_e32 v9, 0, v142, vcc
	v_cndmask_b32_e32 v10, 0, v143, vcc
	v_cndmask_b32_e32 v11, 0, v144, vcc
	v_cvt_pk_bf16_f32 v114, v3, v6
	v_cvt_pk_bf16_f32 v115, v7, v8
	v_cvt_pk_bf16_f32 v116, v9, v10
	v_cndmask_b32_e32 v4, 0, v145, vcc
	v_cvt_pk_bf16_f32 v117, v11, v4
	v_cndmask_b32_e32 v3, 0, v146, vcc
	v_cndmask_b32_e32 v6, 0, v147, vcc
	v_cndmask_b32_e32 v7, 0, v148, vcc
	v_cndmask_b32_e32 v8, 0, v149, vcc
	v_cndmask_b32_e32 v9, 0, v150, vcc
	v_cndmask_b32_e32 v10, 0, v151, vcc
	v_cndmask_b32_e32 v11, 0, v152, vcc
	v_cvt_pk_bf16_f32 v118, v3, v6
	v_cvt_pk_bf16_f32 v119, v7, v8
	v_cvt_pk_bf16_f32 v120, v9, v10
	v_cndmask_b32_e32 v4, 0, v153, vcc
	v_cvt_pk_bf16_f32 v121, v11, v4
	v_cndmask_b32_e32 v3, 0, v154, vcc
	v_cndmask_b32_e32 v6, 0, v155, vcc
	v_cndmask_b32_e32 v7, 0, v156, vcc
	v_cndmask_b32_e32 v8, 0, v157, vcc
	v_cndmask_b32_e32 v9, 0, v158, vcc
	v_cndmask_b32_e32 v10, 0, v159, vcc
	v_cndmask_b32_e32 v11, 0, v160, vcc
	v_cvt_pk_bf16_f32 v122, v3, v6
	v_cvt_pk_bf16_f32 v123, v7, v8
	v_cvt_pk_bf16_f32 v124, v9, v10
	v_cndmask_b32_e32 v4, 0, v161, vcc
	v_cvt_pk_bf16_f32 v125, v11, v4
	v_cndmask_b32_e32 v3, 0, v162, vcc
	v_cndmask_b32_e32 v6, 0, v163, vcc
	v_cndmask_b32_e32 v7, 0, v164, vcc
	v_cndmask_b32_e32 v8, 0, v165, vcc
	v_cndmask_b32_e32 v9, 0, v166, vcc
	v_cndmask_b32_e32 v10, 0, v167, vcc
	v_cvt_pk_bf16_f32 v126, v3, v6
	v_cvt_pk_bf16_f32 v127, v7, v8
	v_cvt_pk_bf16_f32 v128, v9, v10
	v_cndmask_b32_e32 v4, 0, v168, vcc
	v_cndmask_b32_e32 v0, 0, v169, vcc
	v_cvt_pk_bf16_f32 v129, v4, v0
	v_lshl_add_u64 v[0:1], v[132:133], 0, s[88:89]
	v_lshl_add_u64 v[8:9], v[0:1], 4, s[4:5]
	v_add_co_u32_e32 v12, vcc, s54, v8
	global_load_dwordx4 v[4:7], v[8:9], off
	global_load_dwordx4 v[0:3], v[8:9], off offset:1024
	v_addc_co_u32_e32 v13, vcc, 0, v9, vcc
	v_add_co_u32_e32 v14, vcc, s77, v8
	s_nop 1
	v_addc_co_u32_e32 v15, vcc, 0, v9, vcc
	global_load_dwordx4 v[8:11], v[14:15], off offset:-4096
	global_load_dwordx4 v[138:141], v[12:13], off offset:1024
	global_load_dwordx4 v[142:145], v[12:13], off offset:2048
	global_load_dwordx4 v[146:149], v[12:13], off offset:3072
	global_load_dwordx4 v[150:153], v[14:15], off
	global_load_dwordx4 v[154:157], v[14:15], off offset:1024
	global_load_dwordx4 v[158:161], v[14:15], off offset:2048
	s_nop 0
	global_load_dwordx4 v[12:15], v[14:15], off offset:3072
	s_waitcnt vmcnt(9)
	v_mfma_f32_32x32x16_bf16 v[16:31], v[4:7], v[32:35], 0
	s_waitcnt vmcnt(8)
	v_mfma_f32_32x32x16_bf16 v[16:31], v[0:3], v[36:39], v[16:31]
	s_waitcnt vmcnt(7)
	v_mfma_f32_32x32x16_bf16 v[16:31], v[8:11], v[98:101], v[16:31]
	s_waitcnt vmcnt(6)
	v_mfma_f32_32x32x16_bf16 v[16:31], v[138:141], v[102:105], v[16:31]
	s_waitcnt vmcnt(5)
	v_mfma_f32_32x32x16_bf16 v[16:31], v[142:145], v[106:109], v[16:31]
	s_waitcnt vmcnt(4)
	v_mfma_f32_32x32x16_bf16 v[16:31], v[146:149], v[110:113], v[16:31]
	s_waitcnt vmcnt(3)
	v_mfma_f32_32x32x16_bf16 v[16:31], v[150:153], v[114:117], v[16:31]
	s_waitcnt vmcnt(2)
	v_mfma_f32_32x32x16_bf16 v[16:31], v[154:157], v[118:121], v[16:31]
	s_waitcnt vmcnt(1)
	v_mfma_f32_32x32x16_bf16 v[16:31], v[158:161], v[122:125], v[16:31]
	s_waitcnt vmcnt(0)
	v_mfma_f32_32x32x16_bf16 v[16:31], v[12:15], v[126:129], v[16:31]
	s_or_b32 s2, s88, 0x600
	s_mov_b32 s3, s89
	v_lshl_add_u64 v[0:1], v[132:133], 0, s[2:3]
	v_lshl_add_u64 v[4:5], v[0:1], 4, s[4:5]
	v_add_co_u32_e32 v6, vcc, s54, v4
	global_load_dwordx4 v[0:3], v[4:5], off
	global_load_dwordx4 v[138:141], v[4:5], off offset:1024
	global_load_dwordx4 v[142:145], v[4:5], off offset:2048
	global_load_dwordx4 v[146:149], v[4:5], off offset:3072
	v_addc_co_u32_e32 v7, vcc, 0, v5, vcc
	v_add_co_u32_e32 v4, vcc, s77, v4
	s_nop 1
	v_addc_co_u32_e32 v5, vcc, 0, v5, vcc
	global_load_dwordx4 v[150:153], v[6:7], off offset:1024
	global_load_dwordx4 v[154:157], v[6:7], off offset:2048
	global_load_dwordx4 v[158:161], v[4:5], off offset:-4096
	global_load_dwordx4 v[162:165], v[6:7], off offset:3072
	global_load_dwordx4 v[166:169], v[4:5], off
	global_load_dwordx4 v[170:173], v[4:5], off offset:1024
	global_load_dwordx4 v[174:177], v[4:5], off offset:2048
	global_load_dwordx4 v[178:181], v[4:5], off offset:3072
	s_waitcnt vmcnt(11)
	v_mfma_f32_32x32x16_bf16 v[0:15], v[0:3], v[32:35], 0
	s_waitcnt vmcnt(10)
	v_mfma_f32_32x32x16_bf16 v[0:15], v[138:141], v[36:39], v[0:15]
	s_waitcnt vmcnt(9)
	v_mfma_f32_32x32x16_bf16 v[0:15], v[142:145], v[40:43], v[0:15]
	s_waitcnt vmcnt(8)
	v_mfma_f32_32x32x16_bf16 v[0:15], v[146:149], v[44:47], v[0:15]
	s_waitcnt vmcnt(5)
	v_mfma_f32_32x32x16_bf16 v[0:15], v[158:161], v[98:101], v[0:15]
	v_mfma_f32_32x32x16_bf16 v[0:15], v[150:153], v[102:105], v[0:15]
	v_mfma_f32_32x32x16_bf16 v[0:15], v[154:157], v[106:109], v[0:15]
	s_waitcnt vmcnt(4)
	v_mfma_f32_32x32x16_bf16 v[0:15], v[162:165], v[110:113], v[0:15]
	s_waitcnt vmcnt(3)
	v_mfma_f32_32x32x16_bf16 v[0:15], v[166:169], v[114:117], v[0:15]
	s_waitcnt vmcnt(2)
	v_mfma_f32_32x32x16_bf16 v[0:15], v[170:173], v[118:121], v[0:15]
	s_waitcnt vmcnt(1)
	v_mfma_f32_32x32x16_bf16 v[0:15], v[174:177], v[122:125], v[0:15]
	s_waitcnt vmcnt(0)
	v_mfma_f32_32x32x16_bf16 v[0:15], v[178:181], v[126:129], v[0:15]
	v_mul_f32_e32 v96, 0x3d372713, v16
	v_mul_f32_e32 v96, v16, v96
	v_fma_f32 v96, v16, v96, v16
	v_mul_f32_e32 v96, 0x3fcc422a, v96
	v_mul_f32_e32 v96, 0xbfb8aa3b, v96
	v_exp_f32_e32 v96, v96
	v_ashrrev_i32_e32 v135, 31, v134
	v_lshlrev_b64 v[134:135], 1, v[134:135]
	s_or_b32 s2, s88, 0xc00
	v_add_f32_e32 v96, 1.0, v96
	v_rcp_f32_e32 v96, v96
	s_nop 0
	v_mul_f32_e32 v16, v16, v96
	v_mul_f32_e32 v96, 0x3d372713, v17
	v_mul_f32_e32 v96, v17, v96
	v_fma_f32 v96, v17, v96, v17
	v_mul_f32_e32 v96, 0x3fcc422a, v96
	v_mul_f32_e32 v96, 0xbfb8aa3b, v96
	v_exp_f32_e32 v96, v96
	s_nop 0
	v_add_f32_e32 v96, 1.0, v96
	v_rcp_f32_e32 v96, v96
	s_nop 0
	v_mul_f32_e32 v17, v17, v96
	v_mul_f32_e32 v96, 0x3d372713, v18
	v_mul_f32_e32 v96, v18, v96
	v_fma_f32 v96, v18, v96, v18
	v_mul_f32_e32 v96, 0x3fcc422a, v96
	v_mul_f32_e32 v96, 0xbfb8aa3b, v96
	v_exp_f32_e32 v96, v96
	v_cvt_pk_bf16_f32 v16, v16, v17
	s_nop 0
	v_add_f32_e32 v96, 1.0, v96
	v_rcp_f32_e32 v96, v96
	s_nop 0
	v_mul_f32_e32 v18, v18, v96
	v_mul_f32_e32 v96, 0x3d372713, v19
	v_mul_f32_e32 v96, v19, v96
	v_fma_f32 v96, v19, v96, v19
	v_mul_f32_e32 v96, 0x3fcc422a, v96
	v_mul_f32_e32 v96, 0xbfb8aa3b, v96
	v_exp_f32_e32 v96, v96
	s_nop 0
	v_add_f32_e32 v96, 1.0, v96
	v_rcp_f32_e32 v96, v96
	s_nop 0
	v_mul_f32_e32 v19, v19, v96
	v_cvt_pk_bf16_f32 v17, v18, v19
	v_lshlrev_b64 v[18:19], 11, v[130:131]
	v_lshl_add_u64 v[18:19], s[10:11], 0, v[18:19]
	v_lshl_add_u64 v[18:19], v[18:19], 0, v[134:135]
	global_store_dwordx2 v[18:19], v[16:17], off
	v_mul_f32_e32 v16, 0x3d372713, v20
	v_mul_f32_e32 v17, 0x3d372713, v21
	v_mul_f32_e32 v16, v20, v16
	v_mul_f32_e32 v17, v21, v17
	v_fma_f32 v16, v20, v16, v20
	v_fma_f32 v17, v21, v17, v21
	v_mul_f32_e32 v16, 0x3fcc422a, v16
	v_mul_f32_e32 v17, 0x3fcc422a, v17
	v_mul_f32_e32 v16, 0xbfb8aa3b, v16
	v_mul_f32_e32 v17, 0xbfb8aa3b, v17
	v_exp_f32_e32 v16, v16
	v_exp_f32_e32 v17, v17
	v_add_f32_e32 v16, 1.0, v16
	v_add_f32_e32 v17, 1.0, v17
	v_rcp_f32_e32 v16, v16
	v_rcp_f32_e32 v17, v17
	v_mul_f32_e32 v16, v20, v16
	v_mul_f32_e32 v17, v21, v17
	v_mul_f32_e32 v20, 0x3d372713, v22
	v_mul_f32_e32 v21, 0x3d372713, v23
	v_mul_f32_e32 v20, v22, v20
	v_mul_f32_e32 v21, v23, v21
	v_fma_f32 v20, v22, v20, v22
	v_fma_f32 v21, v23, v21, v23
	v_mul_f32_e32 v20, 0x3fcc422a, v20
	v_mul_f32_e32 v21, 0x3fcc422a, v21
	v_mul_f32_e32 v20, 0xbfb8aa3b, v20
	v_mul_f32_e32 v21, 0xbfb8aa3b, v21
	v_exp_f32_e32 v20, v20
	v_exp_f32_e32 v21, v21
	v_cvt_pk_bf16_f32 v16, v16, v17
	v_add_f32_e32 v20, 1.0, v20
	v_add_f32_e32 v21, 1.0, v21
	v_rcp_f32_e32 v20, v20
	v_rcp_f32_e32 v21, v21
	v_mul_f32_e32 v20, v22, v20
	v_mul_f32_e32 v21, v23, v21
	v_cvt_pk_bf16_f32 v17, v20, v21
	global_store_dwordx2 v[18:19], v[16:17], off offset:16
	v_mul_f32_e32 v16, 0x3d372713, v24
	v_mul_f32_e32 v16, v24, v16
	v_fma_f32 v16, v24, v16, v24
	v_mul_f32_e32 v16, 0x3fcc422a, v16
	v_mul_f32_e32 v16, 0xbfb8aa3b, v16
	v_exp_f32_e32 v16, v16
	v_mul_f32_e32 v21, 0x3d372713, v31
	v_mul_f32_e32 v21, v31, v21
	v_fma_f32 v21, v31, v21, v31
	v_add_f32_e32 v16, 1.0, v16
	v_rcp_f32_e32 v16, v16
	v_mul_f32_e32 v21, 0x3fcc422a, v21
	v_mul_f32_e32 v21, 0xbfb8aa3b, v21
	v_exp_f32_e32 v21, v21
	v_mul_f32_e32 v17, v24, v16
	v_mul_f32_e32 v16, 0x3d372713, v25
	v_mul_f32_e32 v16, v25, v16
	v_fma_f32 v16, v25, v16, v25
	v_mul_f32_e32 v16, 0x3fcc422a, v16
	v_mul_f32_e32 v16, 0xbfb8aa3b, v16
	v_exp_f32_e32 v16, v16
	v_add_f32_e32 v21, 1.0, v21
	v_rcp_f32_e32 v21, v21
	v_add_f32_e32 v16, 1.0, v16
	v_rcp_f32_e32 v16, v16
	v_mul_f32_e32 v21, v31, v21
	v_mul_f32_e32 v18, v25, v16
	v_mul_f32_e32 v16, 0x3d372713, v26
	v_mul_f32_e32 v16, v26, v16
	v_fma_f32 v16, v26, v16, v26
	v_mul_f32_e32 v16, 0x3fcc422a, v16
	v_mul_f32_e32 v16, 0xbfb8aa3b, v16
	v_exp_f32_e32 v16, v16
	v_cvt_pk_bf16_f32 v18, v17, v18
	s_nop 0
	v_add_f32_e32 v16, 1.0, v16
	v_rcp_f32_e32 v16, v16
	s_nop 0
	v_mul_f32_e32 v19, v26, v16
	v_mul_f32_e32 v16, 0x3d372713, v27
	v_mul_f32_e32 v16, v27, v16
	v_fma_f32 v16, v27, v16, v27
	v_mul_f32_e32 v16, 0x3fcc422a, v16
	v_mul_f32_e32 v16, 0xbfb8aa3b, v16
	v_exp_f32_e32 v16, v16
	s_nop 0
	v_add_f32_e32 v16, 1.0, v16
	v_rcp_f32_e32 v16, v16
	s_nop 0
	v_mul_f32_e32 v20, v27, v16
	v_or_b32_e32 v16, 1, v130
	v_ashrrev_i32_e32 v17, 31, v16
	v_lshlrev_b64 v[16:17], 11, v[16:17]
	v_lshl_add_u64 v[16:17], s[10:11], 0, v[16:17]
	v_cvt_pk_bf16_f32 v19, v19, v20
	v_lshl_add_u64 v[16:17], v[16:17], 0, v[134:135]
	global_store_dwordx2 v[16:17], v[18:19], off
	v_mul_f32_e32 v18, 0x3d372713, v28
	v_mul_f32_e32 v19, 0x3d372713, v29
	v_mul_f32_e32 v18, v28, v18
	v_mul_f32_e32 v19, v29, v19
	v_mul_f32_e32 v20, 0x3d372713, v30
	v_fma_f32 v18, v28, v18, v28
	v_fma_f32 v19, v29, v19, v29
	v_mul_f32_e32 v20, v30, v20
	v_mul_f32_e32 v18, 0x3fcc422a, v18
	v_mul_f32_e32 v19, 0x3fcc422a, v19
	v_fma_f32 v20, v30, v20, v30
	v_mul_f32_e32 v18, 0xbfb8aa3b, v18
	v_mul_f32_e32 v19, 0xbfb8aa3b, v19
	v_mul_f32_e32 v20, 0x3fcc422a, v20
	v_exp_f32_e32 v18, v18
	v_exp_f32_e32 v19, v19
	v_mul_f32_e32 v20, 0xbfb8aa3b, v20
	v_exp_f32_e32 v20, v20
	v_add_f32_e32 v18, 1.0, v18
	v_add_f32_e32 v19, 1.0, v19
	v_rcp_f32_e32 v18, v18
	v_rcp_f32_e32 v19, v19
	v_add_f32_e32 v20, 1.0, v20
	v_rcp_f32_e32 v20, v20
	v_mul_f32_e32 v18, v28, v18
	v_mul_f32_e32 v19, v29, v19
	v_cvt_pk_bf16_f32 v18, v18, v19
	v_mul_f32_e32 v20, v30, v20
	v_cvt_pk_bf16_f32 v19, v20, v21
	global_store_dwordx2 v[16:17], v[18:19], off offset:16
	v_mul_f32_e32 v17, 0x3d372713, v0
	v_mul_f32_e32 v17, v0, v17
	v_fma_f32 v17, v0, v17, v0
	v_mul_f32_e32 v17, 0x3fcc422a, v17
	v_mul_f32_e32 v17, 0xbfb8aa3b, v17
	v_exp_f32_e32 v17, v17
	v_or_b32_e32 v16, 2, v130
	v_add_f32_e32 v17, 1.0, v17
	v_rcp_f32_e32 v17, v17
	s_nop 0
	v_mul_f32_e32 v0, v0, v17
	v_mul_f32_e32 v17, 0x3d372713, v1
	v_mul_f32_e32 v17, v1, v17
	v_fma_f32 v17, v1, v17, v1
	v_mul_f32_e32 v17, 0x3fcc422a, v17
	v_mul_f32_e32 v17, 0xbfb8aa3b, v17
	v_exp_f32_e32 v17, v17
	s_nop 0
	v_add_f32_e32 v17, 1.0, v17
	v_rcp_f32_e32 v17, v17
	s_nop 0
	v_mul_f32_e32 v1, v1, v17
	v_mul_f32_e32 v17, 0x3d372713, v2
	v_mul_f32_e32 v17, v2, v17
	v_fma_f32 v17, v2, v17, v2
	v_mul_f32_e32 v17, 0x3fcc422a, v17
	v_mul_f32_e32 v17, 0xbfb8aa3b, v17
	v_exp_f32_e32 v17, v17
	v_cvt_pk_bf16_f32 v0, v0, v1
	s_nop 0
	v_add_f32_e32 v17, 1.0, v17
	v_rcp_f32_e32 v17, v17
	s_nop 0
	v_mul_f32_e32 v2, v2, v17
	v_mul_f32_e32 v17, 0x3d372713, v3
	v_mul_f32_e32 v17, v3, v17
	v_fma_f32 v17, v3, v17, v3
	v_mul_f32_e32 v17, 0x3fcc422a, v17
	v_mul_f32_e32 v17, 0xbfb8aa3b, v17
	v_exp_f32_e32 v17, v17
	s_nop 0
	v_add_f32_e32 v17, 1.0, v17
	v_rcp_f32_e32 v17, v17
	s_nop 0
	v_mul_f32_e32 v3, v3, v17
	v_ashrrev_i32_e32 v17, 31, v16
	v_cvt_pk_bf16_f32 v1, v2, v3
	v_lshlrev_b64 v[2:3], 11, v[16:17]
	v_lshl_add_u64 v[2:3], s[10:11], 0, v[2:3]
	v_lshl_add_u64 v[2:3], v[2:3], 0, v[134:135]
	global_store_dwordx2 v[2:3], v[0:1], off
	v_mul_f32_e32 v0, 0x3d372713, v4
	v_mul_f32_e32 v1, 0x3d372713, v5
	v_mul_f32_e32 v0, v4, v0
	v_mul_f32_e32 v1, v5, v1
	v_fma_f32 v0, v4, v0, v4
	v_fma_f32 v1, v5, v1, v5
	v_mul_f32_e32 v0, 0x3fcc422a, v0
	v_mul_f32_e32 v1, 0x3fcc422a, v1
	v_mul_f32_e32 v0, 0xbfb8aa3b, v0
	v_mul_f32_e32 v1, 0xbfb8aa3b, v1
	v_exp_f32_e32 v0, v0
	v_exp_f32_e32 v1, v1
	v_add_f32_e32 v0, 1.0, v0
	v_add_f32_e32 v1, 1.0, v1
	v_rcp_f32_e32 v0, v0
	v_rcp_f32_e32 v1, v1
	v_mul_f32_e32 v0, v4, v0
	v_mul_f32_e32 v1, v5, v1
	v_mul_f32_e32 v4, 0x3d372713, v6
	v_mul_f32_e32 v5, 0x3d372713, v7
	v_mul_f32_e32 v4, v6, v4
	v_mul_f32_e32 v5, v7, v5
	v_fma_f32 v4, v6, v4, v6
	v_fma_f32 v5, v7, v5, v7
	v_mul_f32_e32 v4, 0x3fcc422a, v4
	v_mul_f32_e32 v5, 0x3fcc422a, v5
	v_mul_f32_e32 v4, 0xbfb8aa3b, v4
	v_mul_f32_e32 v5, 0xbfb8aa3b, v5
	v_exp_f32_e32 v4, v4
	v_exp_f32_e32 v5, v5
	v_cvt_pk_bf16_f32 v0, v0, v1
	v_add_f32_e32 v4, 1.0, v4
	v_add_f32_e32 v5, 1.0, v5
	v_rcp_f32_e32 v4, v4
	v_rcp_f32_e32 v5, v5
	v_mul_f32_e32 v4, v6, v4
	v_mul_f32_e32 v5, v7, v5
	v_cvt_pk_bf16_f32 v1, v4, v5
	global_store_dwordx2 v[2:3], v[0:1], off offset:16
	v_mul_f32_e32 v0, 0x3d372713, v8
	v_mul_f32_e32 v0, v8, v0
	v_fma_f32 v0, v8, v0, v8
	v_mul_f32_e32 v0, 0x3fcc422a, v0
	v_mul_f32_e32 v0, 0xbfb8aa3b, v0
	v_exp_f32_e32 v0, v0
	v_mul_f32_e32 v5, 0x3d372713, v15
	v_mul_f32_e32 v5, v15, v5
	v_fma_f32 v5, v15, v5, v15
	v_add_f32_e32 v0, 1.0, v0
	v_rcp_f32_e32 v0, v0
	v_mul_f32_e32 v5, 0x3fcc422a, v5
	v_mul_f32_e32 v5, 0xbfb8aa3b, v5
	v_exp_f32_e32 v5, v5
	v_mul_f32_e32 v1, v8, v0
	v_mul_f32_e32 v0, 0x3d372713, v9
	v_mul_f32_e32 v0, v9, v0
	v_fma_f32 v0, v9, v0, v9
	v_mul_f32_e32 v0, 0x3fcc422a, v0
	v_mul_f32_e32 v0, 0xbfb8aa3b, v0
	v_exp_f32_e32 v0, v0
	v_add_f32_e32 v5, 1.0, v5
	v_rcp_f32_e32 v5, v5
	v_add_f32_e32 v0, 1.0, v0
	v_rcp_f32_e32 v0, v0
	v_mul_f32_e32 v5, v15, v5
	v_mul_f32_e32 v2, v9, v0
	v_mul_f32_e32 v0, 0x3d372713, v10
	v_mul_f32_e32 v0, v10, v0
	v_fma_f32 v0, v10, v0, v10
	v_mul_f32_e32 v0, 0x3fcc422a, v0
	v_mul_f32_e32 v0, 0xbfb8aa3b, v0
	v_exp_f32_e32 v0, v0
	v_cvt_pk_bf16_f32 v2, v1, v2
	s_nop 0
	v_add_f32_e32 v0, 1.0, v0
	v_rcp_f32_e32 v0, v0
	s_nop 0
	v_mul_f32_e32 v3, v10, v0
	v_mul_f32_e32 v0, 0x3d372713, v11
	v_mul_f32_e32 v0, v11, v0
	v_fma_f32 v0, v11, v0, v11
	v_mul_f32_e32 v0, 0x3fcc422a, v0
	v_mul_f32_e32 v0, 0xbfb8aa3b, v0
	v_exp_f32_e32 v0, v0
	s_nop 0
	v_add_f32_e32 v0, 1.0, v0
	v_rcp_f32_e32 v0, v0
	s_nop 0
	v_mul_f32_e32 v4, v11, v0
	v_or_b32_e32 v0, 3, v130
	v_ashrrev_i32_e32 v1, 31, v0
	v_lshlrev_b64 v[0:1], 11, v[0:1]
	v_lshl_add_u64 v[0:1], s[10:11], 0, v[0:1]
	v_cvt_pk_bf16_f32 v3, v3, v4
	v_lshl_add_u64 v[0:1], v[0:1], 0, v[134:135]
	global_store_dwordx2 v[0:1], v[2:3], off
	v_mul_f32_e32 v2, 0x3d372713, v12
	v_mul_f32_e32 v3, 0x3d372713, v13
	v_mul_f32_e32 v2, v12, v2
	v_mul_f32_e32 v3, v13, v3
	v_mul_f32_e32 v4, 0x3d372713, v14
	v_fma_f32 v2, v12, v2, v12
	v_fma_f32 v3, v13, v3, v13
	v_mul_f32_e32 v4, v14, v4
	v_mul_f32_e32 v2, 0x3fcc422a, v2
	v_mul_f32_e32 v3, 0x3fcc422a, v3
	v_fma_f32 v4, v14, v4, v14
	v_mul_f32_e32 v2, 0xbfb8aa3b, v2
	v_mul_f32_e32 v3, 0xbfb8aa3b, v3
	v_mul_f32_e32 v4, 0x3fcc422a, v4
	v_exp_f32_e32 v2, v2
	v_exp_f32_e32 v3, v3
	v_mul_f32_e32 v4, 0xbfb8aa3b, v4
	v_exp_f32_e32 v4, v4
	v_add_f32_e32 v2, 1.0, v2
	v_add_f32_e32 v3, 1.0, v3
	v_rcp_f32_e32 v2, v2
	v_rcp_f32_e32 v3, v3
	v_add_f32_e32 v4, 1.0, v4
	v_rcp_f32_e32 v4, v4
	v_mul_f32_e32 v2, v12, v2
	v_mul_f32_e32 v3, v13, v3
	v_cvt_pk_bf16_f32 v2, v2, v3
	v_mul_f32_e32 v4, v14, v4
	v_cvt_pk_bf16_f32 v3, v4, v5
	global_store_dwordx2 v[0:1], v[2:3], off offset:16
	v_lshl_add_u64 v[0:1], v[132:133], 0, s[2:3]
	v_lshl_add_u64 v[16:17], v[0:1], 4, s[4:5]
	v_add_co_u32_e32 v18, vcc, s81, v16
	global_load_dwordx4 v[0:3], v[16:17], off
	global_load_dwordx4 v[4:7], v[16:17], off offset:1024
	global_load_dwordx4 v[8:11], v[16:17], off offset:2048
	global_load_dwordx4 v[12:15], v[16:17], off offset:3072
	v_addc_co_u32_e32 v19, vcc, 0, v17, vcc
	global_load_dwordx4 v[138:141], v[18:19], off
	global_load_dwordx4 v[142:145], v[18:19], off offset:1024
	v_add_co_u32_e32 v18, vcc, s54, v16
	s_nop 1
	v_addc_co_u32_e32 v19, vcc, 0, v17, vcc
	v_add_co_u32_e32 v16, vcc, s77, v16
	s_nop 1
	v_addc_co_u32_e32 v17, vcc, 0, v17, vcc
	global_load_dwordx4 v[146:149], v[16:17], off offset:-4096
	global_load_dwordx4 v[150:153], v[18:19], off offset:1024
	global_load_dwordx4 v[154:157], v[18:19], off offset:2048
	global_load_dwordx4 v[158:161], v[18:19], off offset:3072
	global_load_dwordx4 v[162:165], v[16:17], off
	global_load_dwordx4 v[166:169], v[16:17], off offset:1024
	global_load_dwordx4 v[170:173], v[16:17], off offset:2048
	global_load_dwordx4 v[174:177], v[16:17], off offset:3072
	s_waitcnt vmcnt(13)
	v_mfma_f32_32x32x16_bf16 v[16:31], v[0:3], v[32:35], 0
	s_waitcnt vmcnt(12)
	v_mfma_f32_32x32x16_bf16 v[16:31], v[4:7], v[36:39], v[16:31]
	s_waitcnt vmcnt(11)
	v_mfma_f32_32x32x16_bf16 v[16:31], v[8:11], v[40:43], v[16:31]
	s_waitcnt vmcnt(10)
	v_mfma_f32_32x32x16_bf16 v[16:31], v[12:15], v[44:47], v[16:31]
	s_waitcnt vmcnt(9)
	v_mfma_f32_32x32x16_bf16 v[16:31], v[138:141], v[48:51], v[16:31]
	s_waitcnt vmcnt(8)
	v_mfma_f32_32x32x16_bf16 v[16:31], v[142:145], v[52:55], v[16:31]
	s_waitcnt vmcnt(7)
	v_mfma_f32_32x32x16_bf16 v[16:31], v[146:149], v[98:101], v[16:31]
	s_waitcnt vmcnt(6)
	v_mfma_f32_32x32x16_bf16 v[16:31], v[150:153], v[102:105], v[16:31]
	s_waitcnt vmcnt(5)
	v_mfma_f32_32x32x16_bf16 v[16:31], v[154:157], v[106:109], v[16:31]
	s_waitcnt vmcnt(4)
	v_mfma_f32_32x32x16_bf16 v[16:31], v[158:161], v[110:113], v[16:31]
	s_waitcnt vmcnt(3)
	v_mfma_f32_32x32x16_bf16 v[16:31], v[162:165], v[114:117], v[16:31]
	s_waitcnt vmcnt(2)
	v_mfma_f32_32x32x16_bf16 v[16:31], v[166:169], v[118:121], v[16:31]
	s_waitcnt vmcnt(1)
	v_mfma_f32_32x32x16_bf16 v[16:31], v[170:173], v[122:125], v[16:31]
	s_waitcnt vmcnt(0)
	v_mfma_f32_32x32x16_bf16 v[16:31], v[174:177], v[126:129], v[16:31]
	s_add_i32 s2, s88, 0x1200
	v_lshl_add_u64 v[0:1], v[132:133], 0, s[2:3]
	v_lshl_add_u64 v[4:5], v[0:1], 4, s[4:5]
	v_add_co_u32_e32 v6, vcc, s81, v4
	global_load_dwordx4 v[0:3], v[4:5], off
	global_load_dwordx4 v[138:141], v[4:5], off offset:1024
	global_load_dwordx4 v[142:145], v[4:5], off offset:2048
	global_load_dwordx4 v[146:149], v[4:5], off offset:3072
	v_addc_co_u32_e32 v7, vcc, 0, v5, vcc
	global_load_dwordx4 v[150:153], v[6:7], off
	global_load_dwordx4 v[154:157], v[6:7], off offset:1024
	global_load_dwordx4 v[158:161], v[6:7], off offset:2048
	global_load_dwordx4 v[162:165], v[6:7], off offset:3072
	v_add_co_u32_e32 v6, vcc, s54, v4
	s_nop 1
	v_addc_co_u32_e32 v7, vcc, 0, v5, vcc
	v_add_co_u32_e32 v4, vcc, s77, v4
	s_nop 1
	v_addc_co_u32_e32 v5, vcc, 0, v5, vcc
	global_load_dwordx4 v[166:169], v[6:7], off offset:1024
	global_load_dwordx4 v[170:173], v[6:7], off offset:2048
	global_load_dwordx4 v[174:177], v[4:5], off offset:-4096
	global_load_dwordx4 v[178:181], v[6:7], off offset:3072
	global_load_dwordx4 v[182:185], v[4:5], off
	global_load_dwordx4 v[186:189], v[4:5], off offset:1024
	global_load_dwordx4 v[190:193], v[4:5], off offset:2048
	global_load_dwordx4 v[194:197], v[4:5], off offset:3072
	s_waitcnt vmcnt(15)
	v_mfma_f32_32x32x16_bf16 v[0:15], v[0:3], v[32:35], 0
	s_waitcnt vmcnt(14)
	v_mfma_f32_32x32x16_bf16 v[0:15], v[138:141], v[36:39], v[0:15]
	s_waitcnt vmcnt(13)
	v_mfma_f32_32x32x16_bf16 v[0:15], v[142:145], v[40:43], v[0:15]
	s_waitcnt vmcnt(12)
	v_mfma_f32_32x32x16_bf16 v[0:15], v[146:149], v[44:47], v[0:15]
	s_waitcnt vmcnt(11)
	v_mfma_f32_32x32x16_bf16 v[0:15], v[150:153], v[48:51], v[0:15]
	s_waitcnt vmcnt(10)
	v_mfma_f32_32x32x16_bf16 v[0:15], v[154:157], v[52:55], v[0:15]
	s_waitcnt vmcnt(9)
	v_mfma_f32_32x32x16_bf16 v[0:15], v[158:161], v[56:59], v[0:15]
	s_waitcnt vmcnt(8)
	v_mfma_f32_32x32x16_bf16 v[0:15], v[162:165], v[60:63], v[0:15]
	s_waitcnt vmcnt(5)
	v_mfma_f32_32x32x16_bf16 v[0:15], v[174:177], v[98:101], v[0:15]
	v_mfma_f32_32x32x16_bf16 v[0:15], v[166:169], v[102:105], v[0:15]
	v_mfma_f32_32x32x16_bf16 v[0:15], v[170:173], v[106:109], v[0:15]
	s_waitcnt vmcnt(4)
	v_mfma_f32_32x32x16_bf16 v[0:15], v[178:181], v[110:113], v[0:15]
	s_waitcnt vmcnt(3)
	v_mfma_f32_32x32x16_bf16 v[0:15], v[182:185], v[114:117], v[0:15]
	s_waitcnt vmcnt(2)
	v_mfma_f32_32x32x16_bf16 v[0:15], v[186:189], v[118:121], v[0:15]
	s_waitcnt vmcnt(1)
	v_mfma_f32_32x32x16_bf16 v[0:15], v[190:193], v[122:125], v[0:15]
	s_waitcnt vmcnt(0)
	v_mfma_f32_32x32x16_bf16 v[0:15], v[194:197], v[126:129], v[0:15]
	v_mul_f32_e32 v96, 0x3d372713, v16
	v_mul_f32_e32 v96, v16, v96
	v_fma_f32 v96, v16, v96, v16
	v_mul_f32_e32 v96, 0x3fcc422a, v96
	v_mul_f32_e32 v96, 0xbfb8aa3b, v96
	v_exp_f32_e32 v96, v96
	v_or_b32_e32 v138, 4, v130
	v_ashrrev_i32_e32 v139, 31, v138
	s_add_i32 s2, s88, 0x1800
	v_add_f32_e32 v96, 1.0, v96
	v_rcp_f32_e32 v96, v96
	s_nop 0
	v_mul_f32_e32 v16, v16, v96
	v_mul_f32_e32 v96, 0x3d372713, v17
	v_mul_f32_e32 v96, v17, v96
	v_fma_f32 v96, v17, v96, v17
	v_mul_f32_e32 v96, 0x3fcc422a, v96
	v_mul_f32_e32 v96, 0xbfb8aa3b, v96
	v_exp_f32_e32 v96, v96
	s_nop 0
	v_add_f32_e32 v96, 1.0, v96
	v_rcp_f32_e32 v96, v96
	s_nop 0
	v_mul_f32_e32 v17, v17, v96
	v_mul_f32_e32 v96, 0x3d372713, v18
	v_mul_f32_e32 v96, v18, v96
	v_fma_f32 v96, v18, v96, v18
	v_mul_f32_e32 v96, 0x3fcc422a, v96
	v_mul_f32_e32 v96, 0xbfb8aa3b, v96
	v_exp_f32_e32 v96, v96
	v_cvt_pk_bf16_f32 v16, v16, v17
	s_nop 0
	v_add_f32_e32 v96, 1.0, v96
	v_rcp_f32_e32 v96, v96
	s_nop 0
	v_mul_f32_e32 v18, v18, v96
	v_mul_f32_e32 v96, 0x3d372713, v19
	v_mul_f32_e32 v96, v19, v96
	v_fma_f32 v96, v19, v96, v19
	v_mul_f32_e32 v96, 0x3fcc422a, v96
	v_mul_f32_e32 v96, 0xbfb8aa3b, v96
	v_exp_f32_e32 v96, v96
	s_nop 0
	v_add_f32_e32 v96, 1.0, v96
	v_rcp_f32_e32 v96, v96
	s_nop 0
	v_mul_f32_e32 v19, v19, v96
	v_cvt_pk_bf16_f32 v17, v18, v19
	v_lshlrev_b64 v[18:19], 11, v[138:139]
	v_lshl_add_u64 v[18:19], s[10:11], 0, v[18:19]
	v_lshl_add_u64 v[18:19], v[18:19], 0, v[134:135]
	global_store_dwordx2 v[18:19], v[16:17], off
	v_mul_f32_e32 v16, 0x3d372713, v20
	v_mul_f32_e32 v17, 0x3d372713, v21
	v_mul_f32_e32 v16, v20, v16
	v_mul_f32_e32 v17, v21, v17
	v_fma_f32 v16, v20, v16, v20
	v_fma_f32 v17, v21, v17, v21
	v_mul_f32_e32 v16, 0x3fcc422a, v16
	v_mul_f32_e32 v17, 0x3fcc422a, v17
	v_mul_f32_e32 v16, 0xbfb8aa3b, v16
	v_mul_f32_e32 v17, 0xbfb8aa3b, v17
	v_exp_f32_e32 v16, v16
	v_exp_f32_e32 v17, v17
	v_add_f32_e32 v16, 1.0, v16
	v_add_f32_e32 v17, 1.0, v17
	v_rcp_f32_e32 v16, v16
	v_rcp_f32_e32 v17, v17
	v_mul_f32_e32 v16, v20, v16
	v_mul_f32_e32 v17, v21, v17
	v_mul_f32_e32 v20, 0x3d372713, v22
	v_mul_f32_e32 v21, 0x3d372713, v23
	v_mul_f32_e32 v20, v22, v20
	v_mul_f32_e32 v21, v23, v21
	v_fma_f32 v20, v22, v20, v22
	v_fma_f32 v21, v23, v21, v23
	v_mul_f32_e32 v20, 0x3fcc422a, v20
	v_mul_f32_e32 v21, 0x3fcc422a, v21
	v_mul_f32_e32 v20, 0xbfb8aa3b, v20
	v_mul_f32_e32 v21, 0xbfb8aa3b, v21
	v_exp_f32_e32 v20, v20
	v_exp_f32_e32 v21, v21
	v_cvt_pk_bf16_f32 v16, v16, v17
	v_add_f32_e32 v20, 1.0, v20
	v_add_f32_e32 v21, 1.0, v21
	v_rcp_f32_e32 v20, v20
	v_rcp_f32_e32 v21, v21
	v_mul_f32_e32 v20, v22, v20
	v_mul_f32_e32 v21, v23, v21
	v_cvt_pk_bf16_f32 v17, v20, v21
	global_store_dwordx2 v[18:19], v[16:17], off offset:16
	v_mul_f32_e32 v16, 0x3d372713, v24
	v_mul_f32_e32 v16, v24, v16
	v_fma_f32 v16, v24, v16, v24
	v_mul_f32_e32 v16, 0x3fcc422a, v16
	v_mul_f32_e32 v16, 0xbfb8aa3b, v16
	v_exp_f32_e32 v16, v16
	v_mul_f32_e32 v21, 0x3d372713, v31
	v_mul_f32_e32 v21, v31, v21
	v_fma_f32 v21, v31, v21, v31
	v_add_f32_e32 v16, 1.0, v16
	v_rcp_f32_e32 v16, v16
	v_mul_f32_e32 v21, 0x3fcc422a, v21
	v_mul_f32_e32 v21, 0xbfb8aa3b, v21
	v_exp_f32_e32 v21, v21
	v_mul_f32_e32 v17, v24, v16
	v_mul_f32_e32 v16, 0x3d372713, v25
	v_mul_f32_e32 v16, v25, v16
	v_fma_f32 v16, v25, v16, v25
	v_mul_f32_e32 v16, 0x3fcc422a, v16
	v_mul_f32_e32 v16, 0xbfb8aa3b, v16
	v_exp_f32_e32 v16, v16
	v_add_f32_e32 v21, 1.0, v21
	v_rcp_f32_e32 v21, v21
	v_add_f32_e32 v16, 1.0, v16
	v_rcp_f32_e32 v16, v16
	v_mul_f32_e32 v21, v31, v21
	v_mul_f32_e32 v18, v25, v16
	v_mul_f32_e32 v16, 0x3d372713, v26
	v_mul_f32_e32 v16, v26, v16
	v_fma_f32 v16, v26, v16, v26
	v_mul_f32_e32 v16, 0x3fcc422a, v16
	v_mul_f32_e32 v16, 0xbfb8aa3b, v16
	v_exp_f32_e32 v16, v16
	v_cvt_pk_bf16_f32 v18, v17, v18
	s_nop 0
	v_add_f32_e32 v16, 1.0, v16
	v_rcp_f32_e32 v16, v16
	s_nop 0
	v_mul_f32_e32 v19, v26, v16
	v_mul_f32_e32 v16, 0x3d372713, v27
	v_mul_f32_e32 v16, v27, v16
	v_fma_f32 v16, v27, v16, v27
	v_mul_f32_e32 v16, 0x3fcc422a, v16
	v_mul_f32_e32 v16, 0xbfb8aa3b, v16
	v_exp_f32_e32 v16, v16
	s_nop 0
	v_add_f32_e32 v16, 1.0, v16
	v_rcp_f32_e32 v16, v16
	s_nop 0
	v_mul_f32_e32 v20, v27, v16
	v_or_b32_e32 v16, 5, v130
	v_ashrrev_i32_e32 v17, 31, v16
	v_lshlrev_b64 v[16:17], 11, v[16:17]
	v_lshl_add_u64 v[16:17], s[10:11], 0, v[16:17]
	v_cvt_pk_bf16_f32 v19, v19, v20
	v_lshl_add_u64 v[16:17], v[16:17], 0, v[134:135]
	global_store_dwordx2 v[16:17], v[18:19], off
	v_mul_f32_e32 v18, 0x3d372713, v28
	v_mul_f32_e32 v19, 0x3d372713, v29
	v_mul_f32_e32 v18, v28, v18
	v_mul_f32_e32 v19, v29, v19
	v_mul_f32_e32 v20, 0x3d372713, v30
	v_fma_f32 v18, v28, v18, v28
	v_fma_f32 v19, v29, v19, v29
	v_mul_f32_e32 v20, v30, v20
	v_mul_f32_e32 v18, 0x3fcc422a, v18
	v_mul_f32_e32 v19, 0x3fcc422a, v19
	v_fma_f32 v20, v30, v20, v30
	v_mul_f32_e32 v18, 0xbfb8aa3b, v18
	v_mul_f32_e32 v19, 0xbfb8aa3b, v19
	v_mul_f32_e32 v20, 0x3fcc422a, v20
	v_exp_f32_e32 v18, v18
	v_exp_f32_e32 v19, v19
	v_mul_f32_e32 v20, 0xbfb8aa3b, v20
	v_exp_f32_e32 v20, v20
	v_add_f32_e32 v18, 1.0, v18
	v_add_f32_e32 v19, 1.0, v19
	v_rcp_f32_e32 v18, v18
	v_rcp_f32_e32 v19, v19
	v_add_f32_e32 v20, 1.0, v20
	v_rcp_f32_e32 v20, v20
	v_mul_f32_e32 v18, v28, v18
	v_mul_f32_e32 v19, v29, v19
	v_cvt_pk_bf16_f32 v18, v18, v19
	v_mul_f32_e32 v20, v30, v20
	v_cvt_pk_bf16_f32 v19, v20, v21
	global_store_dwordx2 v[16:17], v[18:19], off offset:16
	v_mul_f32_e32 v17, 0x3d372713, v0
	v_mul_f32_e32 v17, v0, v17
	v_fma_f32 v17, v0, v17, v0
	v_mul_f32_e32 v17, 0x3fcc422a, v17
	v_mul_f32_e32 v17, 0xbfb8aa3b, v17
	v_exp_f32_e32 v17, v17
	v_or_b32_e32 v16, 6, v130
	v_add_f32_e32 v17, 1.0, v17
	v_rcp_f32_e32 v17, v17
	s_nop 0
	v_mul_f32_e32 v0, v0, v17
	v_mul_f32_e32 v17, 0x3d372713, v1
	v_mul_f32_e32 v17, v1, v17
	v_fma_f32 v17, v1, v17, v1
	v_mul_f32_e32 v17, 0x3fcc422a, v17
	v_mul_f32_e32 v17, 0xbfb8aa3b, v17
	v_exp_f32_e32 v17, v17
	s_nop 0
	v_add_f32_e32 v17, 1.0, v17
	v_rcp_f32_e32 v17, v17
	s_nop 0
	v_mul_f32_e32 v1, v1, v17
	v_mul_f32_e32 v17, 0x3d372713, v2
	v_mul_f32_e32 v17, v2, v17
	v_fma_f32 v17, v2, v17, v2
	v_mul_f32_e32 v17, 0x3fcc422a, v17
	v_mul_f32_e32 v17, 0xbfb8aa3b, v17
	v_exp_f32_e32 v17, v17
	v_cvt_pk_bf16_f32 v0, v0, v1
	s_nop 0
	v_add_f32_e32 v17, 1.0, v17
	v_rcp_f32_e32 v17, v17
	s_nop 0
	v_mul_f32_e32 v2, v2, v17
	v_mul_f32_e32 v17, 0x3d372713, v3
	v_mul_f32_e32 v17, v3, v17
	v_fma_f32 v17, v3, v17, v3
	v_mul_f32_e32 v17, 0x3fcc422a, v17
	v_mul_f32_e32 v17, 0xbfb8aa3b, v17
	v_exp_f32_e32 v17, v17
	s_nop 0
	v_add_f32_e32 v17, 1.0, v17
	v_rcp_f32_e32 v17, v17
	s_nop 0
	v_mul_f32_e32 v3, v3, v17
	v_ashrrev_i32_e32 v17, 31, v16
	v_cvt_pk_bf16_f32 v1, v2, v3
	v_lshlrev_b64 v[2:3], 11, v[16:17]
	v_lshl_add_u64 v[2:3], s[10:11], 0, v[2:3]
	v_lshl_add_u64 v[2:3], v[2:3], 0, v[134:135]
	global_store_dwordx2 v[2:3], v[0:1], off
	v_mul_f32_e32 v0, 0x3d372713, v4
	v_mul_f32_e32 v1, 0x3d372713, v5
	v_mul_f32_e32 v0, v4, v0
	v_mul_f32_e32 v1, v5, v1
	v_fma_f32 v0, v4, v0, v4
	v_fma_f32 v1, v5, v1, v5
	v_mul_f32_e32 v0, 0x3fcc422a, v0
	v_mul_f32_e32 v1, 0x3fcc422a, v1
	v_mul_f32_e32 v0, 0xbfb8aa3b, v0
	v_mul_f32_e32 v1, 0xbfb8aa3b, v1
	v_exp_f32_e32 v0, v0
	v_exp_f32_e32 v1, v1
	v_add_f32_e32 v0, 1.0, v0
	v_add_f32_e32 v1, 1.0, v1
	v_rcp_f32_e32 v0, v0
	v_rcp_f32_e32 v1, v1
	v_mul_f32_e32 v0, v4, v0
	v_mul_f32_e32 v1, v5, v1
	v_mul_f32_e32 v4, 0x3d372713, v6
	v_mul_f32_e32 v5, 0x3d372713, v7
	v_mul_f32_e32 v4, v6, v4
	v_mul_f32_e32 v5, v7, v5
	v_fma_f32 v4, v6, v4, v6
	v_fma_f32 v5, v7, v5, v7
	v_mul_f32_e32 v4, 0x3fcc422a, v4
	v_mul_f32_e32 v5, 0x3fcc422a, v5
	v_mul_f32_e32 v4, 0xbfb8aa3b, v4
	v_mul_f32_e32 v5, 0xbfb8aa3b, v5
	v_exp_f32_e32 v4, v4
	v_exp_f32_e32 v5, v5
	v_cvt_pk_bf16_f32 v0, v0, v1
	v_add_f32_e32 v4, 1.0, v4
	v_add_f32_e32 v5, 1.0, v5
	v_rcp_f32_e32 v4, v4
	v_rcp_f32_e32 v5, v5
	v_mul_f32_e32 v4, v6, v4
	v_mul_f32_e32 v5, v7, v5
	v_cvt_pk_bf16_f32 v1, v4, v5
	global_store_dwordx2 v[2:3], v[0:1], off offset:16
	v_mul_f32_e32 v0, 0x3d372713, v8
	v_mul_f32_e32 v0, v8, v0
	v_fma_f32 v0, v8, v0, v8
	v_mul_f32_e32 v0, 0x3fcc422a, v0
	v_mul_f32_e32 v0, 0xbfb8aa3b, v0
	v_exp_f32_e32 v0, v0
	v_mul_f32_e32 v5, 0x3d372713, v15
	v_mul_f32_e32 v5, v15, v5
	v_fma_f32 v5, v15, v5, v15
	v_add_f32_e32 v0, 1.0, v0
	v_rcp_f32_e32 v0, v0
	v_mul_f32_e32 v5, 0x3fcc422a, v5
	v_mul_f32_e32 v5, 0xbfb8aa3b, v5
	v_exp_f32_e32 v5, v5
	v_mul_f32_e32 v1, v8, v0
	v_mul_f32_e32 v0, 0x3d372713, v9
	v_mul_f32_e32 v0, v9, v0
	v_fma_f32 v0, v9, v0, v9
	v_mul_f32_e32 v0, 0x3fcc422a, v0
	v_mul_f32_e32 v0, 0xbfb8aa3b, v0
	v_exp_f32_e32 v0, v0
	v_add_f32_e32 v5, 1.0, v5
	v_rcp_f32_e32 v5, v5
	v_add_f32_e32 v0, 1.0, v0
	v_rcp_f32_e32 v0, v0
	v_mul_f32_e32 v5, v15, v5
	v_mul_f32_e32 v2, v9, v0
	v_mul_f32_e32 v0, 0x3d372713, v10
	v_mul_f32_e32 v0, v10, v0
	v_fma_f32 v0, v10, v0, v10
	v_mul_f32_e32 v0, 0x3fcc422a, v0
	v_mul_f32_e32 v0, 0xbfb8aa3b, v0
	v_exp_f32_e32 v0, v0
	v_cvt_pk_bf16_f32 v2, v1, v2
	s_nop 0
	v_add_f32_e32 v0, 1.0, v0
	v_rcp_f32_e32 v0, v0
	s_nop 0
	v_mul_f32_e32 v3, v10, v0
	v_mul_f32_e32 v0, 0x3d372713, v11
	v_mul_f32_e32 v0, v11, v0
	v_fma_f32 v0, v11, v0, v11
	v_mul_f32_e32 v0, 0x3fcc422a, v0
	v_mul_f32_e32 v0, 0xbfb8aa3b, v0
	v_exp_f32_e32 v0, v0
	s_nop 0
	v_add_f32_e32 v0, 1.0, v0
	v_rcp_f32_e32 v0, v0
	s_nop 0
	v_mul_f32_e32 v4, v11, v0
	v_or_b32_e32 v0, 7, v130
	v_ashrrev_i32_e32 v1, 31, v0
	v_lshlrev_b64 v[0:1], 11, v[0:1]
	v_lshl_add_u64 v[0:1], s[10:11], 0, v[0:1]
	v_cvt_pk_bf16_f32 v3, v3, v4
	v_lshl_add_u64 v[0:1], v[0:1], 0, v[134:135]
	global_store_dwordx2 v[0:1], v[2:3], off
	v_mul_f32_e32 v2, 0x3d372713, v12
	v_mul_f32_e32 v3, 0x3d372713, v13
	v_mul_f32_e32 v2, v12, v2
	v_mul_f32_e32 v3, v13, v3
	v_mul_f32_e32 v4, 0x3d372713, v14
	v_fma_f32 v2, v12, v2, v12
	v_fma_f32 v3, v13, v3, v13
	v_mul_f32_e32 v4, v14, v4
	v_mul_f32_e32 v2, 0x3fcc422a, v2
	v_mul_f32_e32 v3, 0x3fcc422a, v3
	v_fma_f32 v4, v14, v4, v14
	v_mul_f32_e32 v2, 0xbfb8aa3b, v2
	v_mul_f32_e32 v3, 0xbfb8aa3b, v3
	v_mul_f32_e32 v4, 0x3fcc422a, v4
	v_exp_f32_e32 v2, v2
	v_exp_f32_e32 v3, v3
	v_mul_f32_e32 v4, 0xbfb8aa3b, v4
	v_exp_f32_e32 v4, v4
	v_add_f32_e32 v2, 1.0, v2
	v_add_f32_e32 v3, 1.0, v3
	v_rcp_f32_e32 v2, v2
	v_rcp_f32_e32 v3, v3
	v_add_f32_e32 v4, 1.0, v4
	v_rcp_f32_e32 v4, v4
	v_mul_f32_e32 v2, v12, v2
	v_mul_f32_e32 v3, v13, v3
	v_cvt_pk_bf16_f32 v2, v2, v3
	v_mul_f32_e32 v4, v14, v4
	v_cvt_pk_bf16_f32 v3, v4, v5
	global_store_dwordx2 v[0:1], v[2:3], off offset:16
	v_lshl_add_u64 v[0:1], v[132:133], 0, s[2:3]
	v_lshl_add_u64 v[16:17], v[0:1], 4, s[4:5]
	v_add_co_u32_e32 v18, vcc, s81, v16
	global_load_dwordx4 v[0:3], v[16:17], off
	global_load_dwordx4 v[4:7], v[16:17], off offset:1024
	global_load_dwordx4 v[8:11], v[16:17], off offset:2048
	global_load_dwordx4 v[12:15], v[16:17], off offset:3072
	v_addc_co_u32_e32 v19, vcc, 0, v17, vcc
	v_add_co_u32_e32 v20, vcc, s43, v16
	s_nop 1
	v_addc_co_u32_e32 v21, vcc, 0, v17, vcc
	global_load_dwordx4 v[138:141], v[20:21], off offset:-4096
	global_load_dwordx4 v[142:145], v[18:19], off offset:1024
	global_load_dwordx4 v[146:149], v[18:19], off offset:2048
	global_load_dwordx4 v[150:153], v[18:19], off offset:3072
	global_load_dwordx4 v[154:157], v[20:21], off
	global_load_dwordx4 v[158:161], v[20:21], off offset:1024
	v_add_co_u32_e32 v18, vcc, s54, v16
	s_nop 1
	v_addc_co_u32_e32 v19, vcc, 0, v17, vcc
	v_add_co_u32_e32 v16, vcc, s77, v16
	s_nop 1
	v_addc_co_u32_e32 v17, vcc, 0, v17, vcc
	global_load_dwordx4 v[162:165], v[16:17], off offset:-4096
	global_load_dwordx4 v[166:169], v[18:19], off offset:1024
	global_load_dwordx4 v[170:173], v[18:19], off offset:2048
	global_load_dwordx4 v[174:177], v[18:19], off offset:3072
	global_load_dwordx4 v[178:181], v[16:17], off
	global_load_dwordx4 v[182:185], v[16:17], off offset:1024
	global_load_dwordx4 v[186:189], v[16:17], off offset:2048
	global_load_dwordx4 v[190:193], v[16:17], off offset:3072
	s_waitcnt vmcnt(17)
	v_mfma_f32_32x32x16_bf16 v[16:31], v[0:3], v[32:35], 0
	s_waitcnt vmcnt(16)
	v_mfma_f32_32x32x16_bf16 v[16:31], v[4:7], v[36:39], v[16:31]
	s_waitcnt vmcnt(15)
	v_mfma_f32_32x32x16_bf16 v[16:31], v[8:11], v[40:43], v[16:31]
	s_waitcnt vmcnt(14)
	v_mfma_f32_32x32x16_bf16 v[16:31], v[12:15], v[44:47], v[16:31]
	s_waitcnt vmcnt(13)
	v_mfma_f32_32x32x16_bf16 v[16:31], v[138:141], v[48:51], v[16:31]
	s_waitcnt vmcnt(12)
	v_mfma_f32_32x32x16_bf16 v[16:31], v[142:145], v[52:55], v[16:31]
	s_waitcnt vmcnt(11)
	v_mfma_f32_32x32x16_bf16 v[16:31], v[146:149], v[56:59], v[16:31]
	s_waitcnt vmcnt(10)
	v_mfma_f32_32x32x16_bf16 v[16:31], v[150:153], v[60:63], v[16:31]
	s_waitcnt vmcnt(9)
	v_mfma_f32_32x32x16_bf16 v[16:31], v[154:157], v[64:67], v[16:31]
	s_waitcnt vmcnt(8)
	v_mfma_f32_32x32x16_bf16 v[16:31], v[158:161], v[68:71], v[16:31]
	s_waitcnt vmcnt(7)
	v_mfma_f32_32x32x16_bf16 v[16:31], v[162:165], v[98:101], v[16:31]
	s_waitcnt vmcnt(6)
	v_mfma_f32_32x32x16_bf16 v[16:31], v[166:169], v[102:105], v[16:31]
	s_waitcnt vmcnt(5)
	v_mfma_f32_32x32x16_bf16 v[16:31], v[170:173], v[106:109], v[16:31]
	s_waitcnt vmcnt(4)
	v_mfma_f32_32x32x16_bf16 v[16:31], v[174:177], v[110:113], v[16:31]
	s_waitcnt vmcnt(3)
	v_mfma_f32_32x32x16_bf16 v[16:31], v[178:181], v[114:117], v[16:31]
	s_waitcnt vmcnt(2)
	v_mfma_f32_32x32x16_bf16 v[16:31], v[182:185], v[118:121], v[16:31]
	s_waitcnt vmcnt(1)
	v_mfma_f32_32x32x16_bf16 v[16:31], v[186:189], v[122:125], v[16:31]
	s_waitcnt vmcnt(0)
	v_mfma_f32_32x32x16_bf16 v[16:31], v[190:193], v[126:129], v[16:31]
	s_add_i32 s2, s88, 0x1e00
	v_lshl_add_u64 v[0:1], v[132:133], 0, s[2:3]
	v_lshl_add_u64 v[4:5], v[0:1], 4, s[4:5]
	v_add_co_u32_e32 v6, vcc, s81, v4
	global_load_dwordx4 v[0:3], v[4:5], off
	global_load_dwordx4 v[138:141], v[4:5], off offset:1024
	global_load_dwordx4 v[142:145], v[4:5], off offset:2048
	global_load_dwordx4 v[146:149], v[4:5], off offset:3072
	v_addc_co_u32_e32 v7, vcc, 0, v5, vcc
	v_add_co_u32_e32 v8, vcc, s43, v4
	s_nop 1
	v_addc_co_u32_e32 v9, vcc, 0, v5, vcc
	v_add_co_u32_e32 v10, vcc, s54, v4
	global_load_dwordx4 v[150:153], v[6:7], off offset:1024
	global_load_dwordx4 v[154:157], v[6:7], off offset:2048
	global_load_dwordx4 v[158:161], v[8:9], off offset:-4096
	global_load_dwordx4 v[162:165], v[8:9], off
	global_load_dwordx4 v[166:169], v[8:9], off offset:1024
	global_load_dwordx4 v[170:173], v[8:9], off offset:2048
	v_addc_co_u32_e32 v11, vcc, 0, v5, vcc
	v_add_co_u32_e32 v4, vcc, s77, v4
	s_nop 1
	v_addc_co_u32_e32 v5, vcc, 0, v5, vcc
	global_load_dwordx4 v[174:177], v[8:9], off offset:3072
	global_load_dwordx4 v[178:181], v[4:5], off offset:-4096
	global_load_dwordx4 v[182:185], v[6:7], off offset:3072
	global_load_dwordx4 v[186:189], v[10:11], off offset:1024
	global_load_dwordx4 v[190:193], v[10:11], off offset:2048
	global_load_dwordx4 v[194:197], v[10:11], off offset:3072
	global_load_dwordx4 v[198:201], v[4:5], off
	global_load_dwordx4 v[208:211], v[4:5], off offset:1024
	global_load_dwordx4 v[212:215], v[4:5], off offset:2048
	global_load_dwordx4 v[216:219], v[4:5], off offset:3072
	s_waitcnt vmcnt(19)
	v_mfma_f32_32x32x16_bf16 v[0:15], v[0:3], v[32:35], 0
	s_waitcnt vmcnt(18)
	v_mfma_f32_32x32x16_bf16 v[0:15], v[138:141], v[36:39], v[0:15]
	s_waitcnt vmcnt(17)
	v_mfma_f32_32x32x16_bf16 v[0:15], v[142:145], v[40:43], v[0:15]
	s_waitcnt vmcnt(16)
	v_mfma_f32_32x32x16_bf16 v[0:15], v[146:149], v[44:47], v[0:15]
	s_waitcnt vmcnt(13)
	v_mfma_f32_32x32x16_bf16 v[0:15], v[158:161], v[48:51], v[0:15]
	v_mfma_f32_32x32x16_bf16 v[0:15], v[150:153], v[52:55], v[0:15]
	v_mfma_f32_32x32x16_bf16 v[0:15], v[154:157], v[56:59], v[0:15]
	s_waitcnt vmcnt(7)
	v_mfma_f32_32x32x16_bf16 v[0:15], v[182:185], v[60:63], v[0:15]
	v_mfma_f32_32x32x16_bf16 v[0:15], v[162:165], v[64:67], v[0:15]
	v_mfma_f32_32x32x16_bf16 v[0:15], v[166:169], v[68:71], v[0:15]
	v_mfma_f32_32x32x16_bf16 v[0:15], v[170:173], v[72:75], v[0:15]
	v_mfma_f32_32x32x16_bf16 v[0:15], v[174:177], v[76:79], v[0:15]
	v_mfma_f32_32x32x16_bf16 v[0:15], v[178:181], v[98:101], v[0:15]
	s_waitcnt vmcnt(6)
	v_mfma_f32_32x32x16_bf16 v[0:15], v[186:189], v[102:105], v[0:15]
	s_waitcnt vmcnt(5)
	v_mfma_f32_32x32x16_bf16 v[0:15], v[190:193], v[106:109], v[0:15]
	s_waitcnt vmcnt(4)
	v_mfma_f32_32x32x16_bf16 v[0:15], v[194:197], v[110:113], v[0:15]
	s_waitcnt vmcnt(3)
	v_mfma_f32_32x32x16_bf16 v[0:15], v[198:201], v[114:117], v[0:15]
	s_waitcnt vmcnt(2)
	v_mfma_f32_32x32x16_bf16 v[0:15], v[208:211], v[118:121], v[0:15]
	s_waitcnt vmcnt(1)
	v_mfma_f32_32x32x16_bf16 v[0:15], v[212:215], v[122:125], v[0:15]
	s_waitcnt vmcnt(0)
	v_mfma_f32_32x32x16_bf16 v[0:15], v[216:219], v[126:129], v[0:15]
	v_mul_f32_e32 v96, 0x3d372713, v16
	v_mul_f32_e32 v96, v16, v96
	v_fma_f32 v96, v16, v96, v16
	v_mul_f32_e32 v96, 0x3fcc422a, v96
	v_mul_f32_e32 v96, 0xbfb8aa3b, v96
	v_exp_f32_e32 v96, v96
	v_or_b32_e32 v138, 8, v130
	v_ashrrev_i32_e32 v139, 31, v138
	s_add_i32 s2, s88, 0x2400
	v_add_f32_e32 v96, 1.0, v96
	v_rcp_f32_e32 v96, v96
	s_nop 0
	v_mul_f32_e32 v16, v16, v96
	v_mul_f32_e32 v96, 0x3d372713, v17
	v_mul_f32_e32 v96, v17, v96
	v_fma_f32 v96, v17, v96, v17
	v_mul_f32_e32 v96, 0x3fcc422a, v96
	v_mul_f32_e32 v96, 0xbfb8aa3b, v96
	v_exp_f32_e32 v96, v96
	s_nop 0
	v_add_f32_e32 v96, 1.0, v96
	v_rcp_f32_e32 v96, v96
	s_nop 0
	v_mul_f32_e32 v17, v17, v96
	v_mul_f32_e32 v96, 0x3d372713, v18
	v_mul_f32_e32 v96, v18, v96
	v_fma_f32 v96, v18, v96, v18
	v_mul_f32_e32 v96, 0x3fcc422a, v96
	v_mul_f32_e32 v96, 0xbfb8aa3b, v96
	v_exp_f32_e32 v96, v96
	v_cvt_pk_bf16_f32 v16, v16, v17
	s_nop 0
	v_add_f32_e32 v96, 1.0, v96
	v_rcp_f32_e32 v96, v96
	s_nop 0
	v_mul_f32_e32 v18, v18, v96
	v_mul_f32_e32 v96, 0x3d372713, v19
	v_mul_f32_e32 v96, v19, v96
	v_fma_f32 v96, v19, v96, v19
	v_mul_f32_e32 v96, 0x3fcc422a, v96
	v_mul_f32_e32 v96, 0xbfb8aa3b, v96
	v_exp_f32_e32 v96, v96
	s_nop 0
	v_add_f32_e32 v96, 1.0, v96
	v_rcp_f32_e32 v96, v96
	s_nop 0
	v_mul_f32_e32 v19, v19, v96
	v_cvt_pk_bf16_f32 v17, v18, v19
	v_lshlrev_b64 v[18:19], 11, v[138:139]
	v_lshl_add_u64 v[18:19], s[10:11], 0, v[18:19]
	v_lshl_add_u64 v[18:19], v[18:19], 0, v[134:135]
	global_store_dwordx2 v[18:19], v[16:17], off
	v_mul_f32_e32 v16, 0x3d372713, v20
	v_mul_f32_e32 v17, 0x3d372713, v21
	v_mul_f32_e32 v16, v20, v16
	v_mul_f32_e32 v17, v21, v17
	v_fma_f32 v16, v20, v16, v20
	v_fma_f32 v17, v21, v17, v21
	v_mul_f32_e32 v16, 0x3fcc422a, v16
	v_mul_f32_e32 v17, 0x3fcc422a, v17
	v_mul_f32_e32 v16, 0xbfb8aa3b, v16
	v_mul_f32_e32 v17, 0xbfb8aa3b, v17
	v_exp_f32_e32 v16, v16
	v_exp_f32_e32 v17, v17
	v_add_f32_e32 v16, 1.0, v16
	v_add_f32_e32 v17, 1.0, v17
	v_rcp_f32_e32 v16, v16
	v_rcp_f32_e32 v17, v17
	v_mul_f32_e32 v16, v20, v16
	v_mul_f32_e32 v17, v21, v17
	v_mul_f32_e32 v20, 0x3d372713, v22
	v_mul_f32_e32 v21, 0x3d372713, v23
	v_mul_f32_e32 v20, v22, v20
	v_mul_f32_e32 v21, v23, v21
	v_fma_f32 v20, v22, v20, v22
	v_fma_f32 v21, v23, v21, v23
	v_mul_f32_e32 v20, 0x3fcc422a, v20
	v_mul_f32_e32 v21, 0x3fcc422a, v21
	v_mul_f32_e32 v20, 0xbfb8aa3b, v20
	v_mul_f32_e32 v21, 0xbfb8aa3b, v21
	v_exp_f32_e32 v20, v20
	v_exp_f32_e32 v21, v21
	v_cvt_pk_bf16_f32 v16, v16, v17
	v_add_f32_e32 v20, 1.0, v20
	v_add_f32_e32 v21, 1.0, v21
	v_rcp_f32_e32 v20, v20
	v_rcp_f32_e32 v21, v21
	v_mul_f32_e32 v20, v22, v20
	v_mul_f32_e32 v21, v23, v21
	v_cvt_pk_bf16_f32 v17, v20, v21
	global_store_dwordx2 v[18:19], v[16:17], off offset:16
	v_mul_f32_e32 v16, 0x3d372713, v24
	v_mul_f32_e32 v16, v24, v16
	v_fma_f32 v16, v24, v16, v24
	v_mul_f32_e32 v16, 0x3fcc422a, v16
	v_mul_f32_e32 v16, 0xbfb8aa3b, v16
	v_exp_f32_e32 v16, v16
	v_mul_f32_e32 v21, 0x3d372713, v31
	v_mul_f32_e32 v21, v31, v21
	v_fma_f32 v21, v31, v21, v31
	v_add_f32_e32 v16, 1.0, v16
	v_rcp_f32_e32 v16, v16
	v_mul_f32_e32 v21, 0x3fcc422a, v21
	v_mul_f32_e32 v21, 0xbfb8aa3b, v21
	v_exp_f32_e32 v21, v21
	v_mul_f32_e32 v17, v24, v16
	v_mul_f32_e32 v16, 0x3d372713, v25
	v_mul_f32_e32 v16, v25, v16
	v_fma_f32 v16, v25, v16, v25
	v_mul_f32_e32 v16, 0x3fcc422a, v16
	v_mul_f32_e32 v16, 0xbfb8aa3b, v16
	v_exp_f32_e32 v16, v16
	v_add_f32_e32 v21, 1.0, v21
	v_rcp_f32_e32 v21, v21
	v_add_f32_e32 v16, 1.0, v16
	v_rcp_f32_e32 v16, v16
	v_mul_f32_e32 v21, v31, v21
	v_mul_f32_e32 v18, v25, v16
	v_mul_f32_e32 v16, 0x3d372713, v26
	v_mul_f32_e32 v16, v26, v16
	v_fma_f32 v16, v26, v16, v26
	v_mul_f32_e32 v16, 0x3fcc422a, v16
	v_mul_f32_e32 v16, 0xbfb8aa3b, v16
	v_exp_f32_e32 v16, v16
	v_cvt_pk_bf16_f32 v18, v17, v18
	s_nop 0
	v_add_f32_e32 v16, 1.0, v16
	v_rcp_f32_e32 v16, v16
	s_nop 0
	v_mul_f32_e32 v19, v26, v16
	v_mul_f32_e32 v16, 0x3d372713, v27
	v_mul_f32_e32 v16, v27, v16
	v_fma_f32 v16, v27, v16, v27
	v_mul_f32_e32 v16, 0x3fcc422a, v16
	v_mul_f32_e32 v16, 0xbfb8aa3b, v16
	v_exp_f32_e32 v16, v16
	s_nop 0
	v_add_f32_e32 v16, 1.0, v16
	v_rcp_f32_e32 v16, v16
	s_nop 0
	v_mul_f32_e32 v20, v27, v16
	v_or_b32_e32 v16, 9, v130
	v_ashrrev_i32_e32 v17, 31, v16
	v_lshlrev_b64 v[16:17], 11, v[16:17]
	v_lshl_add_u64 v[16:17], s[10:11], 0, v[16:17]
	v_cvt_pk_bf16_f32 v19, v19, v20
	v_lshl_add_u64 v[16:17], v[16:17], 0, v[134:135]
	global_store_dwordx2 v[16:17], v[18:19], off
	v_mul_f32_e32 v18, 0x3d372713, v28
	v_mul_f32_e32 v19, 0x3d372713, v29
	v_mul_f32_e32 v18, v28, v18
	v_mul_f32_e32 v19, v29, v19
	v_mul_f32_e32 v20, 0x3d372713, v30
	v_fma_f32 v18, v28, v18, v28
	v_fma_f32 v19, v29, v19, v29
	v_mul_f32_e32 v20, v30, v20
	v_mul_f32_e32 v18, 0x3fcc422a, v18
	v_mul_f32_e32 v19, 0x3fcc422a, v19
	v_fma_f32 v20, v30, v20, v30
	v_mul_f32_e32 v18, 0xbfb8aa3b, v18
	v_mul_f32_e32 v19, 0xbfb8aa3b, v19
	v_mul_f32_e32 v20, 0x3fcc422a, v20
	v_exp_f32_e32 v18, v18
	v_exp_f32_e32 v19, v19
	v_mul_f32_e32 v20, 0xbfb8aa3b, v20
	v_exp_f32_e32 v20, v20
	v_add_f32_e32 v18, 1.0, v18
	v_add_f32_e32 v19, 1.0, v19
	v_rcp_f32_e32 v18, v18
	v_rcp_f32_e32 v19, v19
	v_add_f32_e32 v20, 1.0, v20
	v_rcp_f32_e32 v20, v20
	v_mul_f32_e32 v18, v28, v18
	v_mul_f32_e32 v19, v29, v19
	v_cvt_pk_bf16_f32 v18, v18, v19
	v_mul_f32_e32 v20, v30, v20
	v_cvt_pk_bf16_f32 v19, v20, v21
	global_store_dwordx2 v[16:17], v[18:19], off offset:16
	v_mul_f32_e32 v17, 0x3d372713, v0
	v_mul_f32_e32 v17, v0, v17
	v_fma_f32 v17, v0, v17, v0
	v_mul_f32_e32 v17, 0x3fcc422a, v17
	v_mul_f32_e32 v17, 0xbfb8aa3b, v17
	v_exp_f32_e32 v17, v17
	v_or_b32_e32 v16, 10, v130
	v_add_f32_e32 v17, 1.0, v17
	v_rcp_f32_e32 v17, v17
	s_nop 0
	v_mul_f32_e32 v0, v0, v17
	v_mul_f32_e32 v17, 0x3d372713, v1
	v_mul_f32_e32 v17, v1, v17
	v_fma_f32 v17, v1, v17, v1
	v_mul_f32_e32 v17, 0x3fcc422a, v17
	v_mul_f32_e32 v17, 0xbfb8aa3b, v17
	v_exp_f32_e32 v17, v17
	s_nop 0
	v_add_f32_e32 v17, 1.0, v17
	v_rcp_f32_e32 v17, v17
	s_nop 0
	v_mul_f32_e32 v1, v1, v17
	v_mul_f32_e32 v17, 0x3d372713, v2
	v_mul_f32_e32 v17, v2, v17
	v_fma_f32 v17, v2, v17, v2
	v_mul_f32_e32 v17, 0x3fcc422a, v17
	v_mul_f32_e32 v17, 0xbfb8aa3b, v17
	v_exp_f32_e32 v17, v17
	v_cvt_pk_bf16_f32 v0, v0, v1
	s_nop 0
	v_add_f32_e32 v17, 1.0, v17
	v_rcp_f32_e32 v17, v17
	s_nop 0
	v_mul_f32_e32 v2, v2, v17
	v_mul_f32_e32 v17, 0x3d372713, v3
	v_mul_f32_e32 v17, v3, v17
	v_fma_f32 v17, v3, v17, v3
	v_mul_f32_e32 v17, 0x3fcc422a, v17
	v_mul_f32_e32 v17, 0xbfb8aa3b, v17
	v_exp_f32_e32 v17, v17
	s_nop 0
	v_add_f32_e32 v17, 1.0, v17
	v_rcp_f32_e32 v17, v17
	s_nop 0
	v_mul_f32_e32 v3, v3, v17
	v_ashrrev_i32_e32 v17, 31, v16
	v_cvt_pk_bf16_f32 v1, v2, v3
	v_lshlrev_b64 v[2:3], 11, v[16:17]
	v_lshl_add_u64 v[2:3], s[10:11], 0, v[2:3]
	v_lshl_add_u64 v[2:3], v[2:3], 0, v[134:135]
	global_store_dwordx2 v[2:3], v[0:1], off
	v_mul_f32_e32 v0, 0x3d372713, v4
	v_mul_f32_e32 v1, 0x3d372713, v5
	v_mul_f32_e32 v0, v4, v0
	v_mul_f32_e32 v1, v5, v1
	v_fma_f32 v0, v4, v0, v4
	v_fma_f32 v1, v5, v1, v5
	v_mul_f32_e32 v0, 0x3fcc422a, v0
	v_mul_f32_e32 v1, 0x3fcc422a, v1
	v_mul_f32_e32 v0, 0xbfb8aa3b, v0
	v_mul_f32_e32 v1, 0xbfb8aa3b, v1
	v_exp_f32_e32 v0, v0
	v_exp_f32_e32 v1, v1
	v_add_f32_e32 v0, 1.0, v0
	v_add_f32_e32 v1, 1.0, v1
	v_rcp_f32_e32 v0, v0
	v_rcp_f32_e32 v1, v1
	v_mul_f32_e32 v0, v4, v0
	v_mul_f32_e32 v1, v5, v1
	v_mul_f32_e32 v4, 0x3d372713, v6
	v_mul_f32_e32 v5, 0x3d372713, v7
	v_mul_f32_e32 v4, v6, v4
	v_mul_f32_e32 v5, v7, v5
	v_fma_f32 v4, v6, v4, v6
	v_fma_f32 v5, v7, v5, v7
	v_mul_f32_e32 v4, 0x3fcc422a, v4
	v_mul_f32_e32 v5, 0x3fcc422a, v5
	v_mul_f32_e32 v4, 0xbfb8aa3b, v4
	v_mul_f32_e32 v5, 0xbfb8aa3b, v5
	v_exp_f32_e32 v4, v4
	v_exp_f32_e32 v5, v5
	v_cvt_pk_bf16_f32 v0, v0, v1
	v_add_f32_e32 v4, 1.0, v4
	v_add_f32_e32 v5, 1.0, v5
	v_rcp_f32_e32 v4, v4
	v_rcp_f32_e32 v5, v5
	v_mul_f32_e32 v4, v6, v4
	v_mul_f32_e32 v5, v7, v5
	v_cvt_pk_bf16_f32 v1, v4, v5
	global_store_dwordx2 v[2:3], v[0:1], off offset:16
	v_mul_f32_e32 v0, 0x3d372713, v8
	v_mul_f32_e32 v0, v8, v0
	v_fma_f32 v0, v8, v0, v8
	v_mul_f32_e32 v0, 0x3fcc422a, v0
	v_mul_f32_e32 v0, 0xbfb8aa3b, v0
	v_exp_f32_e32 v0, v0
	v_mul_f32_e32 v5, 0x3d372713, v15
	v_mul_f32_e32 v5, v15, v5
	v_fma_f32 v5, v15, v5, v15
	v_add_f32_e32 v0, 1.0, v0
	v_rcp_f32_e32 v0, v0
	v_mul_f32_e32 v5, 0x3fcc422a, v5
	v_mul_f32_e32 v5, 0xbfb8aa3b, v5
	v_exp_f32_e32 v5, v5
	v_mul_f32_e32 v1, v8, v0
	v_mul_f32_e32 v0, 0x3d372713, v9
	v_mul_f32_e32 v0, v9, v0
	v_fma_f32 v0, v9, v0, v9
	v_mul_f32_e32 v0, 0x3fcc422a, v0
	v_mul_f32_e32 v0, 0xbfb8aa3b, v0
	v_exp_f32_e32 v0, v0
	v_add_f32_e32 v5, 1.0, v5
	v_rcp_f32_e32 v5, v5
	v_add_f32_e32 v0, 1.0, v0
	v_rcp_f32_e32 v0, v0
	v_mul_f32_e32 v5, v15, v5
	v_mul_f32_e32 v2, v9, v0
	v_mul_f32_e32 v0, 0x3d372713, v10
	v_mul_f32_e32 v0, v10, v0
	v_fma_f32 v0, v10, v0, v10
	v_mul_f32_e32 v0, 0x3fcc422a, v0
	v_mul_f32_e32 v0, 0xbfb8aa3b, v0
	v_exp_f32_e32 v0, v0
	v_cvt_pk_bf16_f32 v2, v1, v2
	s_nop 0
	v_add_f32_e32 v0, 1.0, v0
	v_rcp_f32_e32 v0, v0
	s_nop 0
	v_mul_f32_e32 v3, v10, v0
	v_mul_f32_e32 v0, 0x3d372713, v11
	v_mul_f32_e32 v0, v11, v0
	v_fma_f32 v0, v11, v0, v11
	v_mul_f32_e32 v0, 0x3fcc422a, v0
	v_mul_f32_e32 v0, 0xbfb8aa3b, v0
	v_exp_f32_e32 v0, v0
	s_nop 0
	v_add_f32_e32 v0, 1.0, v0
	v_rcp_f32_e32 v0, v0
	s_nop 0
	v_mul_f32_e32 v4, v11, v0
	v_or_b32_e32 v0, 11, v130
	v_ashrrev_i32_e32 v1, 31, v0
	v_lshlrev_b64 v[0:1], 11, v[0:1]
	v_lshl_add_u64 v[0:1], s[10:11], 0, v[0:1]
	v_cvt_pk_bf16_f32 v3, v3, v4
	v_lshl_add_u64 v[0:1], v[0:1], 0, v[134:135]
	global_store_dwordx2 v[0:1], v[2:3], off
	v_mul_f32_e32 v2, 0x3d372713, v12
	v_mul_f32_e32 v3, 0x3d372713, v13
	v_mul_f32_e32 v2, v12, v2
	v_mul_f32_e32 v3, v13, v3
	v_mul_f32_e32 v4, 0x3d372713, v14
	v_fma_f32 v2, v12, v2, v12
	v_fma_f32 v3, v13, v3, v13
	v_mul_f32_e32 v4, v14, v4
	v_mul_f32_e32 v2, 0x3fcc422a, v2
	v_mul_f32_e32 v3, 0x3fcc422a, v3
	v_fma_f32 v4, v14, v4, v14
	v_mul_f32_e32 v2, 0xbfb8aa3b, v2
	v_mul_f32_e32 v3, 0xbfb8aa3b, v3
	v_mul_f32_e32 v4, 0x3fcc422a, v4
	v_exp_f32_e32 v2, v2
	v_exp_f32_e32 v3, v3
	v_mul_f32_e32 v4, 0xbfb8aa3b, v4
	v_exp_f32_e32 v4, v4
	v_add_f32_e32 v2, 1.0, v2
	v_add_f32_e32 v3, 1.0, v3
	v_rcp_f32_e32 v2, v2
	v_rcp_f32_e32 v3, v3
	v_add_f32_e32 v4, 1.0, v4
	v_rcp_f32_e32 v4, v4
	v_mul_f32_e32 v2, v12, v2
	v_mul_f32_e32 v3, v13, v3
	v_cvt_pk_bf16_f32 v2, v2, v3
	v_mul_f32_e32 v4, v14, v4
	v_cvt_pk_bf16_f32 v3, v4, v5
	global_store_dwordx2 v[0:1], v[2:3], off offset:16
	v_lshl_add_u64 v[0:1], v[132:133], 0, s[2:3]
	v_lshl_add_u64 v[16:17], v[0:1], 4, s[4:5]
	v_add_co_u32_e32 v18, vcc, s81, v16
	global_load_dwordx4 v[0:3], v[16:17], off
	global_load_dwordx4 v[4:7], v[16:17], off offset:1024
	global_load_dwordx4 v[8:11], v[16:17], off offset:2048
	global_load_dwordx4 v[12:15], v[16:17], off offset:3072
	v_addc_co_u32_e32 v19, vcc, 0, v17, vcc
	v_add_co_u32_e32 v20, vcc, s43, v16
	s_nop 1
	v_addc_co_u32_e32 v21, vcc, 0, v17, vcc
	global_load_dwordx4 v[138:141], v[20:21], off offset:-4096
	global_load_dwordx4 v[142:145], v[18:19], off offset:1024
	global_load_dwordx4 v[146:149], v[18:19], off offset:2048
	global_load_dwordx4 v[150:153], v[18:19], off offset:3072
	global_load_dwordx4 v[154:157], v[20:21], off
	global_load_dwordx4 v[158:161], v[20:21], off offset:1024
	global_load_dwordx4 v[162:165], v[20:21], off offset:2048
	global_load_dwordx4 v[166:169], v[20:21], off offset:3072
	v_add_co_u32_e32 v18, vcc, s72, v16
	s_nop 1
	v_addc_co_u32_e32 v19, vcc, 0, v17, vcc
	v_add_co_u32_e32 v20, vcc, s54, v16
	s_nop 1
	v_addc_co_u32_e32 v21, vcc, 0, v17, vcc
	global_load_dwordx4 v[170:173], v[20:21], off offset:-4096
	global_load_dwordx4 v[174:177], v[18:19], off offset:1024
	global_load_dwordx4 v[178:181], v[20:21], off
	global_load_dwordx4 v[182:185], v[20:21], off offset:1024
	global_load_dwordx4 v[186:189], v[20:21], off offset:2048
	global_load_dwordx4 v[190:193], v[20:21], off offset:3072
	v_add_co_u32_e32 v16, vcc, s77, v16
	s_nop 1
	v_addc_co_u32_e32 v17, vcc, 0, v17, vcc
	global_load_dwordx4 v[194:197], v[16:17], off
	global_load_dwordx4 v[198:201], v[16:17], off offset:1024
	global_load_dwordx4 v[208:211], v[16:17], off offset:2048
	global_load_dwordx4 v[212:215], v[16:17], off offset:3072
	s_waitcnt vmcnt(21)
	v_mfma_f32_32x32x16_bf16 v[16:31], v[0:3], v[32:35], 0
	s_waitcnt vmcnt(20)
	v_mfma_f32_32x32x16_bf16 v[16:31], v[4:7], v[36:39], v[16:31]
	s_waitcnt vmcnt(19)
	v_mfma_f32_32x32x16_bf16 v[16:31], v[8:11], v[40:43], v[16:31]
	s_waitcnt vmcnt(18)
	v_mfma_f32_32x32x16_bf16 v[16:31], v[12:15], v[44:47], v[16:31]
	s_waitcnt vmcnt(17)
	v_mfma_f32_32x32x16_bf16 v[16:31], v[138:141], v[48:51], v[16:31]
	s_waitcnt vmcnt(16)
	v_mfma_f32_32x32x16_bf16 v[16:31], v[142:145], v[52:55], v[16:31]
	s_waitcnt vmcnt(15)
	v_mfma_f32_32x32x16_bf16 v[16:31], v[146:149], v[56:59], v[16:31]
	s_waitcnt vmcnt(14)
	v_mfma_f32_32x32x16_bf16 v[16:31], v[150:153], v[60:63], v[16:31]
	s_waitcnt vmcnt(13)
	v_mfma_f32_32x32x16_bf16 v[16:31], v[154:157], v[64:67], v[16:31]
	s_waitcnt vmcnt(12)
	v_mfma_f32_32x32x16_bf16 v[16:31], v[158:161], v[68:71], v[16:31]
	s_waitcnt vmcnt(11)
	v_mfma_f32_32x32x16_bf16 v[16:31], v[162:165], v[72:75], v[16:31]
	s_waitcnt vmcnt(10)
	v_mfma_f32_32x32x16_bf16 v[16:31], v[166:169], v[76:79], v[16:31]
	s_waitcnt vmcnt(9)
	v_mfma_f32_32x32x16_bf16 v[16:31], v[170:173], v[80:83], v[16:31]
	s_waitcnt vmcnt(8)
	v_mfma_f32_32x32x16_bf16 v[16:31], v[174:177], v[84:87], v[16:31]
	s_waitcnt vmcnt(7)
	v_mfma_f32_32x32x16_bf16 v[16:31], v[178:181], v[98:101], v[16:31]
	s_waitcnt vmcnt(6)
	v_mfma_f32_32x32x16_bf16 v[16:31], v[182:185], v[102:105], v[16:31]
	s_waitcnt vmcnt(5)
	v_mfma_f32_32x32x16_bf16 v[16:31], v[186:189], v[106:109], v[16:31]
	s_waitcnt vmcnt(4)
	v_mfma_f32_32x32x16_bf16 v[16:31], v[190:193], v[110:113], v[16:31]
	s_waitcnt vmcnt(3)
	v_mfma_f32_32x32x16_bf16 v[16:31], v[194:197], v[114:117], v[16:31]
	s_waitcnt vmcnt(2)
	v_mfma_f32_32x32x16_bf16 v[16:31], v[198:201], v[118:121], v[16:31]
	s_waitcnt vmcnt(1)
	v_mfma_f32_32x32x16_bf16 v[16:31], v[208:211], v[122:125], v[16:31]
	s_waitcnt vmcnt(0)
	v_mfma_f32_32x32x16_bf16 v[16:31], v[212:215], v[126:129], v[16:31]
	s_addk_i32 s88, 0x2a00
	v_lshl_add_u64 v[0:1], v[132:133], 0, s[88:89]
	v_lshl_add_u64 v[4:5], v[0:1], 4, s[4:5]
	v_add_co_u32_e32 v6, vcc, s81, v4
	global_load_dwordx4 v[0:3], v[4:5], off
	global_load_dwordx4 v[138:141], v[4:5], off offset:1024
	global_load_dwordx4 v[142:145], v[4:5], off offset:2048
	global_load_dwordx4 v[146:149], v[4:5], off offset:3072
	v_addc_co_u32_e32 v7, vcc, 0, v5, vcc
	v_add_co_u32_e32 v8, vcc, s43, v4
	s_nop 1
	v_addc_co_u32_e32 v9, vcc, 0, v5, vcc
	v_add_co_u32_e32 v10, vcc, s72, v4
	global_load_dwordx4 v[150:153], v[6:7], off offset:1024
	global_load_dwordx4 v[154:157], v[6:7], off offset:2048
	global_load_dwordx4 v[158:161], v[8:9], off offset:-4096
	global_load_dwordx4 v[162:165], v[8:9], off
	global_load_dwordx4 v[166:169], v[8:9], off offset:1024
	global_load_dwordx4 v[170:173], v[8:9], off offset:2048
	v_addc_co_u32_e32 v11, vcc, 0, v5, vcc
	v_add_co_u32_e32 v12, vcc, s54, v4
	s_nop 1
	v_addc_co_u32_e32 v13, vcc, 0, v5, vcc
	global_load_dwordx4 v[174:177], v[8:9], off offset:3072
	global_load_dwordx4 v[178:181], v[12:13], off offset:-4096
	global_load_dwordx4 v[182:185], v[6:7], off offset:3072
	global_load_dwordx4 v[186:189], v[10:11], off offset:1024
	global_load_dwordx4 v[190:193], v[10:11], off offset:2048
	global_load_dwordx4 v[194:197], v[10:11], off offset:3072
	global_load_dwordx4 v[198:201], v[12:13], off
	global_load_dwordx4 v[208:211], v[12:13], off offset:1024
	global_load_dwordx4 v[212:215], v[12:13], off offset:2048
	global_load_dwordx4 v[216:219], v[12:13], off offset:3072
	v_add_co_u32_e32 v4, vcc, s77, v4
	s_nop 1
	v_addc_co_u32_e32 v5, vcc, 0, v5, vcc
	global_load_dwordx4 v[220:223], v[4:5], off
	global_load_dwordx4 v[224:227], v[4:5], off offset:1024
	global_load_dwordx4 v[228:231], v[4:5], off offset:2048
	global_load_dwordx4 v[232:235], v[4:5], off offset:3072
	s_waitcnt vmcnt(23)
	v_mfma_f32_32x32x16_bf16 v[0:15], v[0:3], v[32:35], 0
	s_waitcnt vmcnt(22)
	v_mfma_f32_32x32x16_bf16 v[0:15], v[138:141], v[36:39], v[0:15]
	s_waitcnt vmcnt(21)
	v_mfma_f32_32x32x16_bf16 v[0:15], v[142:145], v[40:43], v[0:15]
	s_waitcnt vmcnt(20)
	v_mfma_f32_32x32x16_bf16 v[0:15], v[146:149], v[44:47], v[0:15]
	s_waitcnt vmcnt(17)
	v_mfma_f32_32x32x16_bf16 v[0:15], v[158:161], v[48:51], v[0:15]
	v_mfma_f32_32x32x16_bf16 v[0:15], v[150:153], v[52:55], v[0:15]
	v_mfma_f32_32x32x16_bf16 v[0:15], v[154:157], v[56:59], v[0:15]
	s_waitcnt vmcnt(11)
	v_mfma_f32_32x32x16_bf16 v[0:15], v[182:185], v[60:63], v[0:15]
	v_mfma_f32_32x32x16_bf16 v[0:15], v[162:165], v[64:67], v[0:15]
	v_mfma_f32_32x32x16_bf16 v[0:15], v[166:169], v[68:71], v[0:15]
	v_mfma_f32_32x32x16_bf16 v[0:15], v[170:173], v[72:75], v[0:15]
	v_mfma_f32_32x32x16_bf16 v[0:15], v[174:177], v[76:79], v[0:15]
	v_mfma_f32_32x32x16_bf16 v[0:15], v[178:181], v[80:83], v[0:15]
	s_waitcnt vmcnt(10)
	v_mfma_f32_32x32x16_bf16 v[0:15], v[186:189], v[84:87], v[0:15]
	s_waitcnt vmcnt(9)
	v_mfma_f32_32x32x16_bf16 v[0:15], v[190:193], v[88:91], v[0:15]
	s_waitcnt vmcnt(8)
	v_mfma_f32_32x32x16_bf16 v[0:15], v[194:197], v[92:95], v[0:15]
	s_waitcnt vmcnt(7)
	v_mfma_f32_32x32x16_bf16 v[0:15], v[198:201], v[98:101], v[0:15]
	s_waitcnt vmcnt(6)
	v_mfma_f32_32x32x16_bf16 v[0:15], v[208:211], v[102:105], v[0:15]
	s_waitcnt vmcnt(5)
	v_mfma_f32_32x32x16_bf16 v[0:15], v[212:215], v[106:109], v[0:15]
	s_waitcnt vmcnt(4)
	v_mfma_f32_32x32x16_bf16 v[0:15], v[216:219], v[110:113], v[0:15]
	s_waitcnt vmcnt(3)
	v_mfma_f32_32x32x16_bf16 v[0:15], v[220:223], v[114:117], v[0:15]
	s_waitcnt vmcnt(2)
	v_mfma_f32_32x32x16_bf16 v[0:15], v[224:227], v[118:121], v[0:15]
	s_waitcnt vmcnt(1)
	v_mfma_f32_32x32x16_bf16 v[0:15], v[228:231], v[122:125], v[0:15]
	s_waitcnt vmcnt(0)
	v_mfma_f32_32x32x16_bf16 v[0:15], v[232:235], v[126:129], v[0:15]
	v_mul_f32_e32 v33, 0x3d372713, v16
	v_mul_f32_e32 v33, v16, v33
	v_fma_f32 v33, v16, v33, v16
	v_mul_f32_e32 v33, 0x3fcc422a, v33
	v_mul_f32_e32 v33, 0xbfb8aa3b, v33
	v_exp_f32_e32 v33, v33
	v_or_b32_e32 v32, 12, v130
	s_add_i32 s14, s14, s83
	s_add_i32 s12, s12, s13
	v_add_f32_e32 v33, 1.0, v33
	v_rcp_f32_e32 v33, v33
	s_cmpk_gt_i32 s14, 0xff
	v_mul_f32_e32 v16, v16, v33
	v_mul_f32_e32 v33, 0x3d372713, v17
	v_mul_f32_e32 v33, v17, v33
	v_fma_f32 v33, v17, v33, v17
	v_mul_f32_e32 v33, 0x3fcc422a, v33
	v_mul_f32_e32 v33, 0xbfb8aa3b, v33
	v_exp_f32_e32 v33, v33
	s_nop 0
	v_add_f32_e32 v33, 1.0, v33
	v_rcp_f32_e32 v33, v33
	s_nop 0
	v_mul_f32_e32 v17, v17, v33
	v_mul_f32_e32 v33, 0x3d372713, v18
	v_mul_f32_e32 v33, v18, v33
	v_fma_f32 v33, v18, v33, v18
	v_mul_f32_e32 v33, 0x3fcc422a, v33
	v_mul_f32_e32 v33, 0xbfb8aa3b, v33
	v_exp_f32_e32 v33, v33
	v_cvt_pk_bf16_f32 v16, v16, v17
	s_nop 0
	v_add_f32_e32 v33, 1.0, v33
	v_rcp_f32_e32 v33, v33
	s_nop 0
	v_mul_f32_e32 v18, v18, v33
	v_mul_f32_e32 v33, 0x3d372713, v19
	v_mul_f32_e32 v33, v19, v33
	v_fma_f32 v33, v19, v33, v19
	v_mul_f32_e32 v33, 0x3fcc422a, v33
	v_mul_f32_e32 v33, 0xbfb8aa3b, v33
	v_exp_f32_e32 v33, v33
	s_nop 0
	v_add_f32_e32 v33, 1.0, v33
	v_rcp_f32_e32 v33, v33
	s_nop 0
	v_mul_f32_e32 v19, v19, v33
	v_ashrrev_i32_e32 v33, 31, v32
	v_cvt_pk_bf16_f32 v17, v18, v19
	v_lshlrev_b64 v[18:19], 11, v[32:33]
	v_lshl_add_u64 v[18:19], s[10:11], 0, v[18:19]
	v_lshl_add_u64 v[18:19], v[18:19], 0, v[134:135]
	global_store_dwordx2 v[18:19], v[16:17], off
	v_mul_f32_e32 v16, 0x3d372713, v20
	v_mul_f32_e32 v17, 0x3d372713, v21
	v_mul_f32_e32 v16, v20, v16
	v_mul_f32_e32 v17, v21, v17
	v_fma_f32 v16, v20, v16, v20
	v_fma_f32 v17, v21, v17, v21
	v_mul_f32_e32 v16, 0x3fcc422a, v16
	v_mul_f32_e32 v17, 0x3fcc422a, v17
	v_mul_f32_e32 v16, 0xbfb8aa3b, v16
	v_mul_f32_e32 v17, 0xbfb8aa3b, v17
	v_exp_f32_e32 v16, v16
	v_exp_f32_e32 v17, v17
	v_add_f32_e32 v16, 1.0, v16
	v_add_f32_e32 v17, 1.0, v17
	v_rcp_f32_e32 v16, v16
	v_rcp_f32_e32 v17, v17
	v_mul_f32_e32 v16, v20, v16
	v_mul_f32_e32 v17, v21, v17
	v_mul_f32_e32 v20, 0x3d372713, v22
	v_mul_f32_e32 v21, 0x3d372713, v23
	v_mul_f32_e32 v20, v22, v20
	v_mul_f32_e32 v21, v23, v21
	v_fma_f32 v20, v22, v20, v22
	v_fma_f32 v21, v23, v21, v23
	v_mul_f32_e32 v20, 0x3fcc422a, v20
	v_mul_f32_e32 v21, 0x3fcc422a, v21
	v_mul_f32_e32 v20, 0xbfb8aa3b, v20
	v_mul_f32_e32 v21, 0xbfb8aa3b, v21
	v_exp_f32_e32 v20, v20
	v_exp_f32_e32 v21, v21
	v_cvt_pk_bf16_f32 v16, v16, v17
	v_add_f32_e32 v20, 1.0, v20
	v_add_f32_e32 v21, 1.0, v21
	v_rcp_f32_e32 v20, v20
	v_rcp_f32_e32 v21, v21
	v_mul_f32_e32 v20, v22, v20
	v_mul_f32_e32 v21, v23, v21
	v_cvt_pk_bf16_f32 v17, v20, v21
	global_store_dwordx2 v[18:19], v[16:17], off offset:16
	v_mul_f32_e32 v16, 0x3d372713, v24
	v_mul_f32_e32 v16, v24, v16
	v_fma_f32 v16, v24, v16, v24
	v_mul_f32_e32 v16, 0x3fcc422a, v16
	v_mul_f32_e32 v16, 0xbfb8aa3b, v16
	v_exp_f32_e32 v16, v16
	v_mul_f32_e32 v21, 0x3d372713, v31
	v_mul_f32_e32 v21, v31, v21
	v_fma_f32 v21, v31, v21, v31
	v_add_f32_e32 v16, 1.0, v16
	v_rcp_f32_e32 v16, v16
	v_mul_f32_e32 v21, 0x3fcc422a, v21
	v_mul_f32_e32 v21, 0xbfb8aa3b, v21
	v_exp_f32_e32 v21, v21
	v_mul_f32_e32 v17, v24, v16
	v_mul_f32_e32 v16, 0x3d372713, v25
	v_mul_f32_e32 v16, v25, v16
	v_fma_f32 v16, v25, v16, v25
	v_mul_f32_e32 v16, 0x3fcc422a, v16
	v_mul_f32_e32 v16, 0xbfb8aa3b, v16
	v_exp_f32_e32 v16, v16
	v_add_f32_e32 v21, 1.0, v21
	v_rcp_f32_e32 v21, v21
	v_add_f32_e32 v16, 1.0, v16
	v_rcp_f32_e32 v16, v16
	v_mul_f32_e32 v21, v31, v21
	v_mul_f32_e32 v18, v25, v16
	v_mul_f32_e32 v16, 0x3d372713, v26
	v_mul_f32_e32 v16, v26, v16
	v_fma_f32 v16, v26, v16, v26
	v_mul_f32_e32 v16, 0x3fcc422a, v16
	v_mul_f32_e32 v16, 0xbfb8aa3b, v16
	v_exp_f32_e32 v16, v16
	v_cvt_pk_bf16_f32 v18, v17, v18
	s_nop 0
	v_add_f32_e32 v16, 1.0, v16
	v_rcp_f32_e32 v16, v16
	s_nop 0
	v_mul_f32_e32 v19, v26, v16
	v_mul_f32_e32 v16, 0x3d372713, v27
	v_mul_f32_e32 v16, v27, v16
	v_fma_f32 v16, v27, v16, v27
	v_mul_f32_e32 v16, 0x3fcc422a, v16
	v_mul_f32_e32 v16, 0xbfb8aa3b, v16
	v_exp_f32_e32 v16, v16
	s_nop 0
	v_add_f32_e32 v16, 1.0, v16
	v_rcp_f32_e32 v16, v16
	s_nop 0
	v_mul_f32_e32 v20, v27, v16
	v_or_b32_e32 v16, 13, v130
	v_ashrrev_i32_e32 v17, 31, v16
	v_lshlrev_b64 v[16:17], 11, v[16:17]
	v_lshl_add_u64 v[16:17], s[10:11], 0, v[16:17]
	v_cvt_pk_bf16_f32 v19, v19, v20
	v_lshl_add_u64 v[16:17], v[16:17], 0, v[134:135]
	global_store_dwordx2 v[16:17], v[18:19], off
	v_mul_f32_e32 v18, 0x3d372713, v28
	v_mul_f32_e32 v19, 0x3d372713, v29
	v_mul_f32_e32 v18, v28, v18
	v_mul_f32_e32 v19, v29, v19
	v_mul_f32_e32 v20, 0x3d372713, v30
	v_fma_f32 v18, v28, v18, v28
	v_fma_f32 v19, v29, v19, v29
	v_mul_f32_e32 v20, v30, v20
	v_mul_f32_e32 v18, 0x3fcc422a, v18
	v_mul_f32_e32 v19, 0x3fcc422a, v19
	v_fma_f32 v20, v30, v20, v30
	v_mul_f32_e32 v18, 0xbfb8aa3b, v18
	v_mul_f32_e32 v19, 0xbfb8aa3b, v19
	v_mul_f32_e32 v20, 0x3fcc422a, v20
	v_exp_f32_e32 v18, v18
	v_exp_f32_e32 v19, v19
	v_mul_f32_e32 v20, 0xbfb8aa3b, v20
	v_exp_f32_e32 v20, v20
	v_add_f32_e32 v18, 1.0, v18
	v_add_f32_e32 v19, 1.0, v19
	v_rcp_f32_e32 v18, v18
	v_rcp_f32_e32 v19, v19
	v_add_f32_e32 v20, 1.0, v20
	v_rcp_f32_e32 v20, v20
	v_mul_f32_e32 v18, v28, v18
	v_mul_f32_e32 v19, v29, v19
	v_cvt_pk_bf16_f32 v18, v18, v19
	v_mul_f32_e32 v20, v30, v20
	v_cvt_pk_bf16_f32 v19, v20, v21
	global_store_dwordx2 v[16:17], v[18:19], off offset:16
	v_mul_f32_e32 v17, 0x3d372713, v0
	v_mul_f32_e32 v17, v0, v17
	v_fma_f32 v17, v0, v17, v0
	v_mul_f32_e32 v17, 0x3fcc422a, v17
	v_mul_f32_e32 v17, 0xbfb8aa3b, v17
	v_exp_f32_e32 v17, v17
	v_or_b32_e32 v16, 14, v130
	v_add_f32_e32 v17, 1.0, v17
	v_rcp_f32_e32 v17, v17
	s_nop 0
	v_mul_f32_e32 v0, v0, v17
	v_mul_f32_e32 v17, 0x3d372713, v1
	v_mul_f32_e32 v17, v1, v17
	v_fma_f32 v17, v1, v17, v1
	v_mul_f32_e32 v17, 0x3fcc422a, v17
	v_mul_f32_e32 v17, 0xbfb8aa3b, v17
	v_exp_f32_e32 v17, v17
	s_nop 0
	v_add_f32_e32 v17, 1.0, v17
	v_rcp_f32_e32 v17, v17
	s_nop 0
	v_mul_f32_e32 v1, v1, v17
	v_mul_f32_e32 v17, 0x3d372713, v2
	v_mul_f32_e32 v17, v2, v17
	v_fma_f32 v17, v2, v17, v2
	v_mul_f32_e32 v17, 0x3fcc422a, v17
	v_mul_f32_e32 v17, 0xbfb8aa3b, v17
	v_exp_f32_e32 v17, v17
	v_cvt_pk_bf16_f32 v0, v0, v1
	s_nop 0
	v_add_f32_e32 v17, 1.0, v17
	v_rcp_f32_e32 v17, v17
	s_nop 0
	v_mul_f32_e32 v2, v2, v17
	v_mul_f32_e32 v17, 0x3d372713, v3
	v_mul_f32_e32 v17, v3, v17
	v_fma_f32 v17, v3, v17, v3
	v_mul_f32_e32 v17, 0x3fcc422a, v17
	v_mul_f32_e32 v17, 0xbfb8aa3b, v17
	v_exp_f32_e32 v17, v17
	s_nop 0
	v_add_f32_e32 v17, 1.0, v17
	v_rcp_f32_e32 v17, v17
	s_nop 0
	v_mul_f32_e32 v3, v3, v17
	v_ashrrev_i32_e32 v17, 31, v16
	v_cvt_pk_bf16_f32 v1, v2, v3
	v_lshlrev_b64 v[2:3], 11, v[16:17]
	v_lshl_add_u64 v[2:3], s[10:11], 0, v[2:3]
	v_lshl_add_u64 v[2:3], v[2:3], 0, v[134:135]
	global_store_dwordx2 v[2:3], v[0:1], off
	v_mul_f32_e32 v0, 0x3d372713, v4
	v_mul_f32_e32 v1, 0x3d372713, v5
	v_mul_f32_e32 v0, v4, v0
	v_mul_f32_e32 v1, v5, v1
	v_fma_f32 v0, v4, v0, v4
	v_fma_f32 v1, v5, v1, v5
	v_mul_f32_e32 v0, 0x3fcc422a, v0
	v_mul_f32_e32 v1, 0x3fcc422a, v1
	v_mul_f32_e32 v0, 0xbfb8aa3b, v0
	v_mul_f32_e32 v1, 0xbfb8aa3b, v1
	v_exp_f32_e32 v0, v0
	v_exp_f32_e32 v1, v1
	v_add_f32_e32 v0, 1.0, v0
	v_add_f32_e32 v1, 1.0, v1
	v_rcp_f32_e32 v0, v0
	v_rcp_f32_e32 v1, v1
	v_mul_f32_e32 v0, v4, v0
	v_mul_f32_e32 v1, v5, v1
	v_mul_f32_e32 v4, 0x3d372713, v6
	v_mul_f32_e32 v5, 0x3d372713, v7
	v_mul_f32_e32 v4, v6, v4
	v_mul_f32_e32 v5, v7, v5
	v_fma_f32 v4, v6, v4, v6
	v_fma_f32 v5, v7, v5, v7
	v_mul_f32_e32 v4, 0x3fcc422a, v4
	v_mul_f32_e32 v5, 0x3fcc422a, v5
	v_mul_f32_e32 v4, 0xbfb8aa3b, v4
	v_mul_f32_e32 v5, 0xbfb8aa3b, v5
	v_exp_f32_e32 v4, v4
	v_exp_f32_e32 v5, v5
	v_cvt_pk_bf16_f32 v0, v0, v1
	v_add_f32_e32 v4, 1.0, v4
	v_add_f32_e32 v5, 1.0, v5
	v_rcp_f32_e32 v4, v4
	v_rcp_f32_e32 v5, v5
	v_mul_f32_e32 v4, v6, v4
	v_mul_f32_e32 v5, v7, v5
	v_cvt_pk_bf16_f32 v1, v4, v5
	global_store_dwordx2 v[2:3], v[0:1], off offset:16
	v_mul_f32_e32 v0, 0x3d372713, v8
	v_mul_f32_e32 v0, v8, v0
	v_fma_f32 v0, v8, v0, v8
	v_mul_f32_e32 v0, 0x3fcc422a, v0
	v_mul_f32_e32 v0, 0xbfb8aa3b, v0
	v_exp_f32_e32 v0, v0
	v_mul_f32_e32 v5, 0x3d372713, v15
	v_mul_f32_e32 v5, v15, v5
	v_fma_f32 v5, v15, v5, v15
	v_add_f32_e32 v0, 1.0, v0
	v_rcp_f32_e32 v0, v0
	v_mul_f32_e32 v5, 0x3fcc422a, v5
	v_mul_f32_e32 v5, 0xbfb8aa3b, v5
	v_exp_f32_e32 v5, v5
	v_mul_f32_e32 v1, v8, v0
	v_mul_f32_e32 v0, 0x3d372713, v9
	v_mul_f32_e32 v0, v9, v0
	v_fma_f32 v0, v9, v0, v9
	v_mul_f32_e32 v0, 0x3fcc422a, v0
	v_mul_f32_e32 v0, 0xbfb8aa3b, v0
	v_exp_f32_e32 v0, v0
	v_add_f32_e32 v5, 1.0, v5
	v_rcp_f32_e32 v5, v5
	v_add_f32_e32 v0, 1.0, v0
	v_rcp_f32_e32 v0, v0
	v_mul_f32_e32 v5, v15, v5
	v_mul_f32_e32 v2, v9, v0
	v_mul_f32_e32 v0, 0x3d372713, v10
	v_mul_f32_e32 v0, v10, v0
	v_fma_f32 v0, v10, v0, v10
	v_mul_f32_e32 v0, 0x3fcc422a, v0
	v_mul_f32_e32 v0, 0xbfb8aa3b, v0
	v_exp_f32_e32 v0, v0
	v_cvt_pk_bf16_f32 v2, v1, v2
	s_nop 0
	v_add_f32_e32 v0, 1.0, v0
	v_rcp_f32_e32 v0, v0
	s_nop 0
	v_mul_f32_e32 v3, v10, v0
	v_mul_f32_e32 v0, 0x3d372713, v11
	v_mul_f32_e32 v0, v11, v0
	v_fma_f32 v0, v11, v0, v11
	v_mul_f32_e32 v0, 0x3fcc422a, v0
	v_mul_f32_e32 v0, 0xbfb8aa3b, v0
	v_exp_f32_e32 v0, v0
	s_nop 0
	v_add_f32_e32 v0, 1.0, v0
	v_rcp_f32_e32 v0, v0
	s_nop 0
	v_mul_f32_e32 v4, v11, v0
	v_or_b32_e32 v0, 15, v130
	v_ashrrev_i32_e32 v1, 31, v0
	v_lshlrev_b64 v[0:1], 11, v[0:1]
	v_lshl_add_u64 v[0:1], s[10:11], 0, v[0:1]
	v_cvt_pk_bf16_f32 v3, v3, v4
	v_lshl_add_u64 v[0:1], v[0:1], 0, v[134:135]
	global_store_dwordx2 v[0:1], v[2:3], off
	v_mul_f32_e32 v2, 0x3d372713, v12
	v_mul_f32_e32 v3, 0x3d372713, v13
	v_mul_f32_e32 v2, v12, v2
	v_mul_f32_e32 v3, v13, v3
	v_mul_f32_e32 v4, 0x3d372713, v14
	v_fma_f32 v2, v12, v2, v12
	v_fma_f32 v3, v13, v3, v13
	v_mul_f32_e32 v4, v14, v4
	v_mul_f32_e32 v2, 0x3fcc422a, v2
	v_mul_f32_e32 v3, 0x3fcc422a, v3
	v_fma_f32 v4, v14, v4, v14
	v_mul_f32_e32 v2, 0xbfb8aa3b, v2
	v_mul_f32_e32 v3, 0xbfb8aa3b, v3
	v_mul_f32_e32 v4, 0x3fcc422a, v4
	v_exp_f32_e32 v2, v2
	v_exp_f32_e32 v3, v3
	v_mul_f32_e32 v4, 0xbfb8aa3b, v4
	v_exp_f32_e32 v4, v4
	v_add_f32_e32 v2, 1.0, v2
	v_add_f32_e32 v3, 1.0, v3
	v_rcp_f32_e32 v2, v2
	v_rcp_f32_e32 v3, v3
	v_add_f32_e32 v4, 1.0, v4
	v_rcp_f32_e32 v4, v4
	v_mul_f32_e32 v2, v12, v2
	v_mul_f32_e32 v3, v13, v3
	v_cvt_pk_bf16_f32 v2, v2, v3
	v_mul_f32_e32 v4, v14, v4
	v_cvt_pk_bf16_f32 v3, v4, v5
	global_store_dwordx2 v[0:1], v[2:3], off offset:16
	s_cbranch_scc0 .LBB0_447
